# NSA importance arrays IA/IB: per-row column rotation removes 32-way LDS bank conflicts in lane-per-token writes
# speedup vs baseline: 1.0105x; 1.0065x over previous
; #define LAS __attribute__((address_space(3)))
; __device__ __forceinline__ int kperm(int key) { return (key & ~12) | ((key & 4) << 1) | ((key & 8) >> 1); }
; __device__ __forceinline__ void unit(LAS unsigned char* lds, const bf16* Z, const bf16* kct, const bf16* vct, bf16* OAp, int b, int g, int iq, const int tid_in) {
;     int tid = tid_in; asm volatile("" : "+v"(tid));
;     const int lane = tid & 63, r32 = lane & 31, hi = lane >> 5; const int w = __builtin_amdgcn_readfirstlane(tid >> 6);
;     const int j = w >> 1, hq = 4 * g + j, tl = 32 * (w & 1) + r32, t0 = 64 * iq, t = t0 + tl;
;     const size_t rowZ = (size_t)(b * T + t) * ZLD;
;     LAS bf16* KS = (LAS bf16*)(lds + L_KS); LAS bf16* VT = (LAS bf16*)(lds + L_VT); LAS bf16* KC = (LAS bf16*)(lds + L_KC); LAS bf16* VC = (LAS bf16*)(lds + L_VC);
;     LAS float* IA = (LAS float*)(lds + L_IA); LAS float* IB = (LAS float*)(lds + L_IB); LAS unsigned* MSK = (LAS unsigned*)(lds + L_MASK); LAS int* TL = (LAS int*)(lds + L_TL);
;     bf16x8 qr[4];
; #pragma unroll
;     for (int d0 = 0; d0 < 4; ++d0) qr[d0] = *(const bf16x8*)(Z + rowZ + ZQ + hq * 64 + 16 * d0 + 8 * hi);
;     const float slope2 = __builtin_amdgcn_exp2f(-0.5f * (float)(hq + 1)) * LOG2E;
;     float gate[3];
; #pragma unroll
;     for (int x = 0; x < 3; ++x) gate[x] = sigmoidf_(bf2f(Z[rowZ + ZNG + hq * 3 + x]));
;     f32x16 otot[2];
; #pragma unroll
;     for (int r = 0; r < 16; ++r) { otot[0][r] = 0.f; otot[1][r] = 0.f; }
;     {
;         const bf16* kc = kct + (size_t)((b * 4 + g) * 128) * 64; const bf16* vc = vct + (size_t)((b * 4 + g) * 128) * 64;
; #pragma unroll
;         for (int q = 0; q < 2; ++q) { const int idx = tid + 512 * q, key = idx >> 3, ch = idx & 7;
;             const v4u kv = *(const v4u*)(kc + key * 64 + ch * 8); *(LAS v4u*)(KC + key * KST + ch * 8) = kv;
;             const v4u vv = *(const v4u*)(vc + key * 64 + ch * 8); const int pos = kperm(key);
;             const unsigned ww[4] = {vv.x, vv.y, vv.z, vv.w};
; #pragma unroll
;             for (int e = 0; e < 4; ++e) { VC[(ch * 8 + 2 * e) * VST2 + pos] = (bf16)(ww[e] & 0xffffu); VC[(ch * 8 + 2 * e + 1) * VST2 + pos] = (bf16)(ww[e] >> 16); } }
;     }
;     __syncthreads();
;     {
;         f32x16 p[4];
; #pragma unroll
;         for (int blk = 0; blk < 4; ++blk) {
; #pragma unroll
;             for (int r = 0; r < 16; ++r) p[blk][r] = 0.f;
; #pragma unroll
.LBB0_416:
	v_mov_b32_e32 v78, v123
	s_and_b32 s23, s4, 3
	s_ashr_i32 s5, s4, 2
	v_readfirstlane_b32 s0, v78
	v_and_b32_e32 v73, 31, v78
	s_ashr_i32 s4, s0, 7
	s_lshl_b32 s1, s23, 2
	s_lshr_b32 s0, s0, 1
	s_add_i32 s6, s4, s1
	v_and_or_b32 v68, s0, 32, v73
	v_readlane_b32 s0, v253, 32
	v_lshl_or_b32 v77, s18, 6, v68
	s_lshl_b32 s22, s5, 11
	v_readlane_b32 s1, v253, 33
	v_or_b32_e32 v118, s22, v77
	s_lshl_b32 s16, s6, 6
	v_mov_b64_e32 v[2:3], s[0:1]
	v_mad_i64_i32 v[2:3], s[0:1], v118, s26, v[2:3]
	s_add_i32 s0, s6, 1
	v_bfe_u32 v74, v78, 5, 1
	s_ashr_i32 s17, s16, 31
	v_cvt_f32_i32_e32 v1, s0
	s_mul_i32 s0, s6, 3
	v_lshl_add_u64 v[4:5], s[16:17], 1, v[2:3]
	v_lshlrev_b32_e32 v120, 4, v74
	v_mov_b32_e32 v121, v187
	s_ashr_i32 s1, s0, 31
	v_lshl_add_u64 v[4:5], v[4:5], 0, v[120:121]
	v_lshl_add_u64 v[2:3], s[0:1], 1, v[2:3]
	s_mov_b64 s[0:1], 0x1400
	global_load_dwordx4 v[98:101], v[4:5], off
	global_load_dwordx4 v[102:105], v[4:5], off offset:32
	global_load_dwordx4 v[106:109], v[4:5], off offset:64
	global_load_dwordx4 v[110:113], v[4:5], off offset:96
	v_lshl_add_u64 v[4:5], v[2:3], 0, s[0:1]
	s_lshl_b32 s0, s5, 9
	s_lshl_b32 s28, s23, 7
	v_add_co_u32_e32 v2, vcc, s97, v2
	s_or_b32 s0, s28, s0
	s_nop 0
	v_addc_co_u32_e32 v3, vcc, 0, v3, vcc
	s_ashr_i32 s1, s0, 31
	global_load_dword v69, v[2:3], off offset:1024
	global_load_ushort v121, v[4:5], off offset:4
	s_lshl_b64 s[0:1], s[0:1], 7
	v_readlane_b32 s5, v252, 0
	v_lshlrev_b32_e32 v2, 3, v78
	v_ashrrev_i32_e32 v119, 3, v78
	s_add_u32 s6, s5, s0
	v_readlane_b32 s5, v252, 1
	v_and_b32_e32 v9, 56, v2
	v_lshlrev_b32_e32 v2, 6, v119
	s_addc_u32 s7, s5, s1
	v_lshlrev_b32_e32 v186, 1, v9
	v_ashrrev_i32_e32 v3, 31, v2
	v_lshl_add_u64 v[6:7], s[6:7], 0, v[186:187]
	v_lshlrev_b64 v[12:13], 1, v[2:3]
	v_lshl_add_u64 v[2:3], v[6:7], 0, v[12:13]
	global_load_dwordx4 v[200:203], v[2:3], off
	v_readlane_b32 s5, v252, 4
	s_add_u32 s0, s5, s0
	v_readlane_b32 s5, v252, 5
	s_addc_u32 s1, s5, s1
	v_add_u32_e32 v8, 0, v186
	s_movk_i32 s5, 0x90
	v_lshl_add_u64 v[10:11], s[0:1], 0, v[186:187]
	v_mad_u64_u32 v[14:15], s[0:1], v119, s5, v[8:9]
	s_movk_i32 s0, 0x10e
	s_nop 0
	v_mad_u32_u24 v9, v9, s0, v8
	v_lshl_add_u64 v[2:3], v[10:11], 0, v[12:13]
	global_load_dwordx4 v[204:207], v[2:3], off
	v_add_u32_e32 v2, 0x200, v78
	v_ashrrev_i32_e32 v15, 3, v2
	v_lshlrev_b32_e32 v2, 6, v15
	v_ashrrev_i32_e32 v3, 31, v2
	v_lshlrev_b64 v[2:3], 1, v[2:3]
	v_lshl_add_u64 v[4:5], v[6:7], 0, v[2:3]
	global_load_dwordx4 v[208:211], v[4:5], off
	v_lshl_add_u64 v[4:5], v[10:11], 0, v[2:3]
	global_load_dwordx4 v[212:215], v[4:5], off
	v_add_u32_e32 v76, 0, v120
	v_mad_u32_u24 v66, v73, s5, v76
	v_mul_f32_e32 v1, -0.5, v1
	v_exp_f32_e32 v1, v1
	v_lshlrev_b32_e32 v122, 2, v74
	v_and_b32_e32 v79, 63, v78
	v_cmp_eq_u32_e64 s[44:45], 0, v73
	v_mul_f32_e32 v124, 0x3fb8aa3b, v1
	v_lshlrev_b32_e32 v5, 1, v119
	v_lshrrev_b32_e32 v12, 1, v119
	v_and_b32_e32 v4, 0x7ffffff3, v119
	v_and_b32_e32 v5, 8, v5
	v_and_b32_e32 v12, 4, v12
	v_or3_b32 v4, v5, v4, v12
	v_lshl_add_u32 v12, v4, 1, v9
	v_mad_u64_u32 v[6:7], s[0:1], v15, s5, v[8:9]
	v_lshlrev_b32_e32 v5, 1, v15
	v_lshrrev_b32_e32 v13, 1, v15
	v_and_b32_e32 v4, 0x7ffffff3, v15
	v_and_b32_e32 v5, 8, v5
	v_and_b32_e32 v13, 4, v13
	v_or3_b32 v4, v5, v4, v13
	v_lshl_add_u32 v13, v4, 1, v9
	s_mov_b32 s5, 0xff800000
	v_cmp_gt_u32_e64 s[0:1], 32, v79
	s_waitcnt vmcnt(3)
	ds_write_b128 v14, v[200:203] offset:18432
	s_waitcnt vmcnt(2)
	ds_write_b16 v12, v204 offset:36864
	ds_write_b16_d16_hi v12, v204 offset:37136
	ds_write_b16 v12, v205 offset:37408
	ds_write_b16_d16_hi v12, v205 offset:37680
	ds_write_b16 v12, v206 offset:37952
	ds_write_b16_d16_hi v12, v206 offset:38224
	ds_write_b16 v12, v207 offset:38496
	ds_write_b16_d16_hi v12, v207 offset:38768
	s_waitcnt vmcnt(1)
	ds_write_b128 v6, v[208:211] offset:18432
	s_waitcnt vmcnt(0)
	ds_write_b16 v13, v212 offset:36864
	ds_write_b16_d16_hi v13, v212 offset:37136
	ds_write_b16 v13, v213 offset:37408
	ds_write_b16_d16_hi v13, v213 offset:37680
	ds_write_b16 v13, v214 offset:37952
	ds_write_b16_d16_hi v13, v214 offset:38224
	ds_write_b16 v13, v215 offset:38496
	ds_write_b16_d16_hi v13, v215 offset:38768
	s_waitcnt lgkmcnt(0)
	s_barrier
	ds_read_b128 v[2:5], v66 offset:18432
	ds_read_b128 v[6:9], v66 offset:18464
	s_waitcnt lgkmcnt(1)
	v_mfma_f32_32x32x16_bf16 v[50:65], v[2:5], v[98:101], 0
	ds_read_b128 v[2:5], v66 offset:18496
	ds_read_b128 v[80:83], v66 offset:32288
	s_waitcnt lgkmcnt(2)
	v_mfma_f32_32x32x16_bf16 v[50:65], v[6:9], v[102:105], v[50:65]
	s_waitcnt lgkmcnt(1)
	v_mfma_f32_32x32x16_bf16 v[50:65], v[2:5], v[106:109], v[50:65]
	ds_read_b128 v[2:5], v66 offset:18528
	s_waitcnt lgkmcnt(0)
	v_mfma_f32_32x32x16_bf16 v[50:65], v[2:5], v[110:113], v[50:65]
	ds_read_b128 v[2:5], v66 offset:23040
	s_waitcnt lgkmcnt(0)
	v_mfma_f32_32x32x16_bf16 v[34:49], v[2:5], v[98:101], 0
	ds_read_b128 v[2:5], v66 offset:23072
	s_waitcnt lgkmcnt(0)
	v_mfma_f32_32x32x16_bf16 v[34:49], v[2:5], v[102:105], v[34:49]
	ds_read_b128 v[2:5], v66 offset:23104
	s_waitcnt lgkmcnt(0)
	v_mfma_f32_32x32x16_bf16 v[34:49], v[2:5], v[106:109], v[34:49]
	ds_read_b128 v[2:5], v66 offset:23136
	s_waitcnt lgkmcnt(0)
	v_mfma_f32_32x32x16_bf16 v[34:49], v[2:5], v[110:113], v[34:49]
	ds_read_b128 v[2:5], v66 offset:27648
	s_waitcnt lgkmcnt(0)
	v_mfma_f32_32x32x16_bf16 v[18:33], v[2:5], v[98:101], 0
	ds_read_b128 v[2:5], v66 offset:27680
	s_waitcnt lgkmcnt(0)
	v_mfma_f32_32x32x16_bf16 v[18:33], v[2:5], v[102:105], v[18:33]
	ds_read_b128 v[2:5], v66 offset:27712
	s_waitcnt lgkmcnt(0)
	v_mfma_f32_32x32x16_bf16 v[18:33], v[2:5], v[106:109], v[18:33]
	ds_read_b128 v[2:5], v66 offset:27744
	s_waitcnt lgkmcnt(0)
; #define LAS __attribute__((address_space(3)))
; __device__ __forceinline__ int crow(int r, int hi) { return (r & 3) + 8 * (r >> 2) + 4 * hi; }
; #define MFMA32(a, b, c) __builtin_amdgcn_mfma_f32_32x32x16_bf16((a), (b), (c), 0, 0, 0)
; __device__ __forceinline__ void unit(LAS unsigned char* lds, const bf16* Z, const bf16* kct, const bf16* vct, bf16* OAp, int b, int g, int iq, const int tid_in) {
;     ...
;             for (int d0 = 0; d0 < 4; ++d0) { const bf16x8 kf = *(const LAS bf16x8*)(KC + (32 * blk + r32) * KST + 16 * d0 + 8 * hi); p[blk] = MFMA32(kf, qr[d0], p[blk]); }
;         }
;         float mx = -INFINITY;
; #pragma unroll
;         for (int blk = 0; blk < 4; ++blk)
; #pragma unroll
;             for (int r = 0; r < 16; ++r) { const int c = 32 * blk + crow(r, hi); const int dist = t - (16 * c + 31); const bool ok = (dist >= 0) && (c < 127);
;                 const float s = ok ? p[blk][r] - slope2 * (float)dist : -INFINITY; p[blk][r] = s; mx = fmaxf(mx, s); }
	v_mfma_f32_32x32x16_bf16 v[18:33], v[2:5], v[110:113], v[18:33]
	ds_read_b128 v[2:5], v66 offset:32256
	s_waitcnt lgkmcnt(0)
	v_mfma_f32_32x32x16_bf16 v[2:17], v[2:5], v[98:101], 0
	v_mfma_f32_32x32x16_bf16 v[2:17], v[80:83], v[102:105], v[2:17]
	ds_read_b128 v[80:83], v66 offset:32320
	s_waitcnt lgkmcnt(0)
	v_mfma_f32_32x32x16_bf16 v[2:17], v[80:83], v[106:109], v[2:17]
	ds_read_b128 v[80:83], v66 offset:32352
	s_waitcnt lgkmcnt(0)
	v_mfma_f32_32x32x16_bf16 v[2:17], v[80:83], v[110:113], v[2:17]
	v_subrev_u32_e32 v80, 31, v77
	v_lshlrev_b32_e32 v81, 6, v74
	v_sub_u32_e32 v1, v80, v81
	v_cmp_lt_i32_e32 vcc, -1, v1
	v_cvt_f32_u32_e32 v1, v1
	v_fma_f32 v1, -v124, v1, v50
	v_cndmask_b32_e32 v66, v229, v1, vcc
	v_or_b32_e32 v1, 16, v81
	v_sub_u32_e32 v1, v80, v1
	v_cmp_lt_i32_e32 vcc, -1, v1
	v_cvt_f32_u32_e32 v1, v1
	v_or_b32_e32 v50, 2, v122
	v_lshlrev_b32_e32 v71, 4, v50
	v_sub_u32_e32 v71, v80, v71
	v_fma_f32 v1, -v124, v1, v51
	v_cndmask_b32_e32 v67, v229, v1, vcc
	v_cmp_lt_i32_e32 vcc, -1, v71
	v_cvt_f32_u32_e32 v71, v71
	v_or_b32_e32 v1, 3, v122
	v_max3_f32 v70, v66, s5, v67
	v_mov_b32_e32 v51, v122
	v_fma_f32 v52, -v124, v71, v52
	v_lshlrev_b32_e32 v71, 4, v1
	v_sub_u32_e32 v71, v80, v71
	v_cndmask_b32_e32 v52, v229, v52, vcc
	v_cmp_lt_i32_e32 vcc, -1, v71
	v_cvt_f32_u32_e32 v71, v71
	v_fma_f32 v53, -v124, v71, v53
	v_cndmask_b32_e32 v53, v229, v53, vcc
	v_max3_f32 v71, v70, v52, v53
	v_or_b32_e32 v70, 8, v122
	v_lshlrev_b32_e32 v72, 4, v70
	v_sub_u32_e32 v72, v80, v72
	v_cmp_lt_i32_e32 vcc, -1, v72
	v_cvt_f32_u32_e32 v72, v72
	v_fma_f32 v54, -v124, v72, v54
	v_or_b32_e32 v72, 0x90, v81
	v_sub_u32_e32 v72, v80, v72
	v_cndmask_b32_e32 v54, v229, v54, vcc
	v_cmp_lt_i32_e32 vcc, -1, v72
	v_cvt_f32_u32_e32 v72, v72
	v_fma_f32 v55, -v124, v72, v55
	v_or_b32_e32 v72, 0xa0, v81
	v_sub_u32_e32 v72, v80, v72
	v_cndmask_b32_e32 v55, v229, v55, vcc
	v_cmp_lt_i32_e32 vcc, -1, v72
	v_cvt_f32_u32_e32 v72, v72
	v_max3_f32 v71, v71, v54, v55
	v_fma_f32 v56, -v124, v72, v56
	v_or_b32_e32 v72, 0xb0, v81
	v_sub_u32_e32 v72, v80, v72
	v_cndmask_b32_e32 v56, v229, v56, vcc
	v_cmp_lt_i32_e32 vcc, -1, v72
	v_cvt_f32_u32_e32 v72, v72
	v_fma_f32 v57, -v124, v72, v57
	v_cndmask_b32_e32 v57, v229, v57, vcc
	v_max3_f32 v72, v71, v56, v57
	v_or_b32_e32 v71, 16, v122
	v_lshlrev_b32_e32 v75, 4, v71
	v_sub_u32_e32 v75, v80, v75
	v_cmp_lt_i32_e32 vcc, -1, v75
	v_cvt_f32_u32_e32 v75, v75
	v_fma_f32 v58, -v124, v75, v58
	v_or_b32_e32 v75, 0x110, v81
	v_sub_u32_e32 v75, v80, v75
	v_cndmask_b32_e32 v58, v229, v58, vcc
	v_cmp_lt_i32_e32 vcc, -1, v75
	v_cvt_f32_u32_e32 v75, v75
	v_fma_f32 v59, -v124, v75, v59
	v_or_b32_e32 v75, 0x120, v81
	v_sub_u32_e32 v75, v80, v75
	v_cndmask_b32_e32 v59, v229, v59, vcc
	v_cmp_lt_i32_e32 vcc, -1, v75
	v_cvt_f32_u32_e32 v75, v75
	v_max3_f32 v72, v72, v58, v59
	v_fma_f32 v60, -v124, v75, v60
	v_or_b32_e32 v75, 0x130, v81
	v_sub_u32_e32 v75, v80, v75
	v_cndmask_b32_e32 v60, v229, v60, vcc
	v_cmp_lt_i32_e32 vcc, -1, v75
	v_cvt_f32_u32_e32 v75, v75
	v_fma_f32 v61, -v124, v75, v61
	v_cndmask_b32_e32 v61, v229, v61, vcc
	v_max3_f32 v75, v72, v60, v61
	v_or_b32_e32 v72, 24, v122
	v_lshlrev_b32_e32 v82, 4, v72
	v_sub_u32_e32 v82, v80, v82
	v_cmp_lt_i32_e32 vcc, -1, v82
	v_cvt_f32_u32_e32 v82, v82
	v_fma_f32 v62, -v124, v82, v62
	v_or_b32_e32 v82, 0x190, v81
	v_sub_u32_e32 v82, v80, v82
	v_cndmask_b32_e32 v62, v229, v62, vcc
	v_cmp_lt_i32_e32 vcc, -1, v82
	v_cvt_f32_u32_e32 v82, v82
	v_fma_f32 v63, -v124, v82, v63
	v_or_b32_e32 v82, 0x1a0, v81
	v_sub_u32_e32 v82, v80, v82
	v_cndmask_b32_e32 v63, v229, v63, vcc
	v_cmp_lt_i32_e32 vcc, -1, v82
	v_cvt_f32_u32_e32 v82, v82
	v_max3_f32 v75, v75, v62, v63
	v_fma_f32 v64, -v124, v82, v64
	v_or_b32_e32 v82, 0x1b0, v81
	v_sub_u32_e32 v82, v80, v82
	v_cndmask_b32_e32 v64, v229, v64, vcc
	v_cmp_lt_i32_e32 vcc, -1, v82
	v_cvt_f32_u32_e32 v82, v82
	v_fma_f32 v65, -v124, v82, v65
	v_cndmask_b32_e32 v65, v229, v65, vcc
	v_max3_f32 v82, v75, v64, v65
	v_or_b32_e32 v75, 32, v122
	v_lshlrev_b32_e32 v83, 4, v75
	v_sub_u32_e32 v83, v80, v83
	v_cmp_lt_i32_e32 vcc, -1, v83
	v_cvt_f32_u32_e32 v83, v83
	v_fma_f32 v34, -v124, v83, v34
	v_or_b32_e32 v83, 0x210, v81
	v_sub_u32_e32 v83, v80, v83
	v_cndmask_b32_e32 v34, v229, v34, vcc
	v_cmp_lt_i32_e32 vcc, -1, v83
	v_cvt_f32_u32_e32 v83, v83
	v_fma_f32 v35, -v124, v83, v35
	v_or_b32_e32 v83, 0x220, v81
	v_sub_u32_e32 v83, v80, v83
	v_cndmask_b32_e32 v35, v229, v35, vcc
	v_cmp_lt_i32_e32 vcc, -1, v83
	v_cvt_f32_u32_e32 v83, v83
	v_max3_f32 v82, v82, v34, v35
	v_fma_f32 v36, -v124, v83, v36
	v_or_b32_e32 v83, 0x230, v81
	v_sub_u32_e32 v83, v80, v83
	v_cndmask_b32_e32 v36, v229, v36, vcc
	v_cmp_lt_i32_e32 vcc, -1, v83
	v_cvt_f32_u32_e32 v83, v83
	v_fma_f32 v37, -v124, v83, v37
	v_or_b32_e32 v83, 0x280, v81
	v_sub_u32_e32 v83, v80, v83
	v_cndmask_b32_e32 v37, v229, v37, vcc
	v_cmp_lt_i32_e32 vcc, -1, v83
	v_cvt_f32_u32_e32 v83, v83
	v_max3_f32 v82, v82, v36, v37
	v_fma_f32 v38, -v124, v83, v38
	v_or_b32_e32 v83, 0x290, v81
	v_sub_u32_e32 v83, v80, v83
	v_cndmask_b32_e32 v38, v229, v38, vcc
	v_cmp_lt_i32_e32 vcc, -1, v83
	v_cvt_f32_u32_e32 v83, v83
	v_fma_f32 v39, -v124, v83, v39
	v_or_b32_e32 v83, 0x2a0, v81
	v_sub_u32_e32 v83, v80, v83
	v_cndmask_b32_e32 v39, v229, v39, vcc
	v_cmp_lt_i32_e32 vcc, -1, v83
	v_cvt_f32_u32_e32 v83, v83
	v_max3_f32 v82, v82, v38, v39
	v_fma_f32 v40, -v124, v83, v40
	v_or_b32_e32 v83, 0x2b0, v81
	v_sub_u32_e32 v83, v80, v83
	v_cndmask_b32_e32 v40, v229, v40, vcc
	v_cmp_lt_i32_e32 vcc, -1, v83
	v_cvt_f32_u32_e32 v83, v83
	v_fma_f32 v41, -v124, v83, v41
	v_or_b32_e32 v83, 0x300, v81
	v_sub_u32_e32 v83, v80, v83
	v_cndmask_b32_e32 v41, v229, v41, vcc
; __device__ __forceinline__ int crow(int r, int hi) { return (r & 3) + 8 * (r >> 2) + 4 * hi; }
; __device__ __forceinline__ void unit(LAS unsigned char* lds, const bf16* Z, const bf16* kct, const bf16* vct, bf16* OAp, int b, int g, int iq, const int tid_in) {
;     ...
;             for (int r = 0; r < 16; ++r) { const int c = 32 * blk + crow(r, hi); const int dist = t - (16 * c + 31); const bool ok = (dist >= 0) && (c < 127);
;                 const float s = ok ? p[blk][r] - slope2 * (float)dist : -INFINITY; p[blk][r] = s; mx = fmaxf(mx, s); }
	v_cmp_lt_i32_e32 vcc, -1, v83
	v_cvt_f32_u32_e32 v83, v83
	v_max3_f32 v82, v82, v40, v41
	v_fma_f32 v42, -v124, v83, v42
	v_or_b32_e32 v83, 0x310, v81
	v_sub_u32_e32 v83, v80, v83
	v_cndmask_b32_e32 v42, v229, v42, vcc
	v_cmp_lt_i32_e32 vcc, -1, v83
	v_cvt_f32_u32_e32 v83, v83
	v_fma_f32 v43, -v124, v83, v43
	v_or_b32_e32 v83, 0x320, v81
	v_sub_u32_e32 v83, v80, v83
	v_cndmask_b32_e32 v43, v229, v43, vcc
	v_cmp_lt_i32_e32 vcc, -1, v83
	v_cvt_f32_u32_e32 v83, v83
	v_max3_f32 v82, v82, v42, v43
	v_fma_f32 v44, -v124, v83, v44
	v_or_b32_e32 v83, 0x330, v81
	v_sub_u32_e32 v83, v80, v83
	v_cndmask_b32_e32 v44, v229, v44, vcc
	v_cmp_lt_i32_e32 vcc, -1, v83
	v_cvt_f32_u32_e32 v83, v83
	v_fma_f32 v45, -v124, v83, v45
	v_or_b32_e32 v83, 0x380, v81
	v_sub_u32_e32 v83, v80, v83
	v_cndmask_b32_e32 v45, v229, v45, vcc
	v_cmp_lt_i32_e32 vcc, -1, v83
	v_cvt_f32_u32_e32 v83, v83
	v_max3_f32 v82, v82, v44, v45
	v_fma_f32 v46, -v124, v83, v46
	v_or_b32_e32 v83, 0x390, v81
	v_sub_u32_e32 v83, v80, v83
	v_cndmask_b32_e32 v46, v229, v46, vcc
	v_cmp_lt_i32_e32 vcc, -1, v83
	v_cvt_f32_u32_e32 v83, v83
	v_fma_f32 v47, -v124, v83, v47
	v_or_b32_e32 v83, 0x3a0, v81
	v_sub_u32_e32 v83, v80, v83
	v_cndmask_b32_e32 v47, v229, v47, vcc
	v_cmp_lt_i32_e32 vcc, -1, v83
	v_cvt_f32_u32_e32 v83, v83
	v_max3_f32 v82, v82, v46, v47
	v_fma_f32 v48, -v124, v83, v48
	v_or_b32_e32 v83, 0x3b0, v81
	v_sub_u32_e32 v83, v80, v83
	v_cndmask_b32_e32 v48, v229, v48, vcc
	v_cmp_lt_i32_e32 vcc, -1, v83
	v_cvt_f32_u32_e32 v83, v83
	v_fma_f32 v49, -v124, v83, v49
	v_cndmask_b32_e32 v49, v229, v49, vcc
	v_max3_f32 v84, v82, v48, v49
	v_or_b32_e32 v82, 0x400, v81
	v_sub_u32_e32 v82, v80, v82
	v_cmp_lt_i32_e32 vcc, -1, v82
	v_cvt_f32_u32_e32 v82, v82
	v_fma_f32 v18, -v124, v82, v18
	v_cndmask_b32_e32 v82, v229, v18, vcc
	v_or_b32_e32 v18, 0x410, v81
	v_sub_u32_e32 v18, v80, v18
	v_cmp_lt_i32_e32 vcc, -1, v18
	v_cvt_f32_u32_e32 v18, v18
	v_fma_f32 v18, -v124, v18, v19
	v_or_b32_e32 v19, 0x420, v81
	v_sub_u32_e32 v19, v80, v19
	v_cndmask_b32_e32 v83, v229, v18, vcc
	v_cmp_lt_i32_e32 vcc, -1, v19
	v_cvt_f32_u32_e32 v19, v19
	v_max3_f32 v18, v84, v82, v83
	v_fma_f32 v19, -v124, v19, v20
	v_cndmask_b32_e32 v84, v229, v19, vcc
	v_or_b32_e32 v19, 0x430, v81
	v_sub_u32_e32 v19, v80, v19
	v_cmp_lt_i32_e32 vcc, -1, v19
	v_cvt_f32_u32_e32 v19, v19
	v_fma_f32 v19, -v124, v19, v21
	v_cndmask_b32_e32 v85, v229, v19, vcc
	v_or_b32_e32 v19, 0x480, v81
	v_sub_u32_e32 v19, v80, v19
	v_cmp_lt_i32_e32 vcc, -1, v19
	v_cvt_f32_u32_e32 v19, v19
	v_max3_f32 v18, v18, v84, v85
	v_fma_f32 v19, -v124, v19, v22
	v_cndmask_b32_e32 v86, v229, v19, vcc
	v_or_b32_e32 v19, 0x490, v81
	v_sub_u32_e32 v19, v80, v19
	v_cmp_lt_i32_e32 vcc, -1, v19
	v_cvt_f32_u32_e32 v19, v19
	v_fma_f32 v19, -v124, v19, v23
	v_cndmask_b32_e32 v87, v229, v19, vcc
	v_or_b32_e32 v19, 0x4a0, v81
	v_sub_u32_e32 v19, v80, v19
	v_cmp_lt_i32_e32 vcc, -1, v19
	v_cvt_f32_u32_e32 v19, v19
	v_max3_f32 v18, v18, v86, v87
	v_fma_f32 v19, -v124, v19, v24
	v_cndmask_b32_e32 v24, v229, v19, vcc
	v_or_b32_e32 v19, 0x4b0, v81
	v_sub_u32_e32 v19, v80, v19
	v_cmp_lt_i32_e32 vcc, -1, v19
	v_cvt_f32_u32_e32 v19, v19
	v_fma_f32 v19, -v124, v19, v25
	v_cndmask_b32_e32 v25, v229, v19, vcc
	v_or_b32_e32 v19, 0x500, v81
	v_sub_u32_e32 v19, v80, v19
	v_cmp_lt_i32_e32 vcc, -1, v19
	v_cvt_f32_u32_e32 v19, v19
	v_max3_f32 v18, v18, v24, v25
	v_fma_f32 v19, -v124, v19, v26
	v_cndmask_b32_e32 v26, v229, v19, vcc
	v_or_b32_e32 v19, 0x510, v81
	v_sub_u32_e32 v19, v80, v19
	v_cmp_lt_i32_e32 vcc, -1, v19
	v_cvt_f32_u32_e32 v19, v19
	v_fma_f32 v19, -v124, v19, v27
	v_cndmask_b32_e32 v27, v229, v19, vcc
	v_or_b32_e32 v19, 0x520, v81
	v_sub_u32_e32 v19, v80, v19
	v_cmp_lt_i32_e32 vcc, -1, v19
	v_cvt_f32_u32_e32 v19, v19
	v_max3_f32 v18, v18, v26, v27
	v_fma_f32 v19, -v124, v19, v28
	v_cndmask_b32_e32 v28, v229, v19, vcc
	v_or_b32_e32 v19, 0x530, v81
	v_sub_u32_e32 v19, v80, v19
	v_cmp_lt_i32_e32 vcc, -1, v19
	v_cvt_f32_u32_e32 v19, v19
	v_fma_f32 v19, -v124, v19, v29
	v_cndmask_b32_e32 v29, v229, v19, vcc
	v_or_b32_e32 v19, 0x580, v81
	v_sub_u32_e32 v19, v80, v19
	v_cmp_lt_i32_e32 vcc, -1, v19
	v_cvt_f32_u32_e32 v19, v19
	v_max3_f32 v18, v18, v28, v29
	v_fma_f32 v19, -v124, v19, v30
	v_cndmask_b32_e32 v30, v229, v19, vcc
	v_or_b32_e32 v19, 0x590, v81
	v_sub_u32_e32 v19, v80, v19
	v_cmp_lt_i32_e32 vcc, -1, v19
	v_cvt_f32_u32_e32 v19, v19
	v_fma_f32 v19, -v124, v19, v31
	v_cndmask_b32_e32 v31, v229, v19, vcc
	v_or_b32_e32 v19, 0x5a0, v81
	v_sub_u32_e32 v19, v80, v19
	v_cmp_lt_i32_e32 vcc, -1, v19
	v_cvt_f32_u32_e32 v19, v19
	v_max3_f32 v18, v18, v30, v31
	v_fma_f32 v19, -v124, v19, v32
	v_cndmask_b32_e32 v32, v229, v19, vcc
	v_or_b32_e32 v19, 0x5b0, v81
	v_sub_u32_e32 v19, v80, v19
	v_cmp_lt_i32_e32 vcc, -1, v19
	v_cvt_f32_u32_e32 v19, v19
	v_fma_f32 v19, -v124, v19, v33
	v_cndmask_b32_e32 v33, v229, v19, vcc
	v_or_b32_e32 v19, 0x600, v81
	v_sub_u32_e32 v19, v80, v19
	v_cmp_lt_i32_e32 vcc, -1, v19
	v_cvt_f32_u32_e32 v19, v19
	v_max3_f32 v18, v18, v32, v33
	v_fma_f32 v2, -v124, v19, v2
	v_cndmask_b32_e32 v88, v229, v2, vcc
	v_or_b32_e32 v2, 0x610, v81
	v_sub_u32_e32 v2, v80, v2
	v_cmp_lt_i32_e32 vcc, -1, v2
	v_cvt_f32_u32_e32 v2, v2
	v_fma_f32 v2, -v124, v2, v3
	v_or_b32_e32 v3, 0x620, v81
	v_sub_u32_e32 v3, v80, v3
	v_cndmask_b32_e32 v89, v229, v2, vcc
	v_cmp_lt_i32_e32 vcc, -1, v3
	v_cvt_f32_u32_e32 v3, v3
	v_max3_f32 v2, v18, v88, v89
	v_fma_f32 v3, -v124, v3, v4
	v_cndmask_b32_e32 v90, v229, v3, vcc
	v_or_b32_e32 v3, 0x630, v81
	v_sub_u32_e32 v3, v80, v3
	v_cmp_lt_i32_e32 vcc, -1, v3
	v_cvt_f32_u32_e32 v3, v3
	v_and_b32_e32 v4, 64, v228
	v_fma_f32 v3, -v124, v3, v5
; __device__ __forceinline__ int crow(int r, int hi) { return (r & 3) + 8 * (r >> 2) + 4 * hi; }
; __device__ __forceinline__ void unit(LAS unsigned char* lds, const bf16* Z, const bf16* kct, const bf16* vct, bf16* OAp, int b, int g, int iq, const int tid_in) {
;     ...
;             for (int r = 0; r < 16; ++r) { const int c = 32 * blk + crow(r, hi); const int dist = t - (16 * c + 31); const bool ok = (dist >= 0) && (c < 127);
;                 const float s = ok ? p[blk][r] - slope2 * (float)dist : -INFINITY; p[blk][r] = s; mx = fmaxf(mx, s); }
;         mx = fmaxf(mx, __shfl_xor(mx, 32));
;         const float msafe = (mx == -INFINITY) ? 0.f : mx;
;         float l = 0.f;
; #pragma unroll
;         for (int blk = 0; blk < 4; ++blk)
; #pragma unroll
;             for (int r = 0; r < 16; ++r) { const float e = __builtin_amdgcn_exp2f(p[blk][r] - msafe); p[blk][r] = e; l += e; }
	v_cndmask_b32_e32 v91, v229, v3, vcc
	v_or_b32_e32 v3, 0x680, v81
	v_sub_u32_e32 v3, v80, v3
	v_cmp_lt_i32_e32 vcc, -1, v3
	v_cvt_f32_u32_e32 v3, v3
	v_max3_f32 v2, v2, v90, v91
	v_fma_f32 v3, -v124, v3, v6
	v_cndmask_b32_e32 v92, v229, v3, vcc
	v_or_b32_e32 v3, 0x690, v81
	v_sub_u32_e32 v3, v80, v3
	v_cmp_lt_i32_e32 vcc, -1, v3
	v_cvt_f32_u32_e32 v3, v3
	v_fma_f32 v3, -v124, v3, v7
	v_cndmask_b32_e32 v93, v229, v3, vcc
	v_or_b32_e32 v3, 0x6a0, v81
	v_sub_u32_e32 v3, v80, v3
	v_cmp_lt_i32_e32 vcc, -1, v3
	v_cvt_f32_u32_e32 v3, v3
	v_max3_f32 v2, v2, v92, v93
	v_fma_f32 v3, -v124, v3, v8
	v_cndmask_b32_e32 v94, v229, v3, vcc
	v_or_b32_e32 v3, 0x6b0, v81
	v_sub_u32_e32 v3, v80, v3
	v_cmp_lt_i32_e32 vcc, -1, v3
	v_cvt_f32_u32_e32 v3, v3
	v_fma_f32 v3, -v124, v3, v9
	v_cndmask_b32_e32 v95, v229, v3, vcc
	v_or_b32_e32 v3, 0x700, v81
	v_sub_u32_e32 v3, v80, v3
	v_cmp_lt_i32_e32 vcc, -1, v3
	v_cvt_f32_u32_e32 v3, v3
	v_max3_f32 v2, v2, v94, v95
	v_fma_f32 v3, -v124, v3, v10
	v_cndmask_b32_e32 v96, v229, v3, vcc
	v_or_b32_e32 v3, 0x710, v81
	v_sub_u32_e32 v3, v80, v3
	v_cmp_lt_i32_e32 vcc, -1, v3
	v_cvt_f32_u32_e32 v3, v3
	v_fma_f32 v3, -v124, v3, v11
	v_cndmask_b32_e32 v97, v229, v3, vcc
	v_or_b32_e32 v3, 0x720, v81
	v_sub_u32_e32 v3, v80, v3
	v_cmp_lt_i32_e32 vcc, -1, v3
	v_cvt_f32_u32_e32 v3, v3
	v_max3_f32 v2, v2, v96, v97
	v_fma_f32 v3, -v124, v3, v12
	v_cndmask_b32_e32 v114, v229, v3, vcc
	v_or_b32_e32 v3, 0x730, v81
	v_sub_u32_e32 v3, v80, v3
	v_cmp_lt_i32_e32 vcc, -1, v3
	v_cvt_f32_u32_e32 v3, v3
	v_fma_f32 v3, -v124, v3, v13
	v_cndmask_b32_e32 v115, v229, v3, vcc
	v_or_b32_e32 v3, 0x780, v81
	v_sub_u32_e32 v3, v80, v3
	v_cmp_lt_i32_e32 vcc, -1, v3
	v_cvt_f32_u32_e32 v3, v3
	v_max3_f32 v2, v2, v114, v115
	v_fma_f32 v3, -v124, v3, v14
	v_cndmask_b32_e32 v116, v229, v3, vcc
	v_or_b32_e32 v3, 0x790, v81
	v_sub_u32_e32 v3, v80, v3
	v_cmp_lt_i32_e32 vcc, -1, v3
	v_cvt_f32_u32_e32 v3, v3
	v_fma_f32 v3, -v124, v3, v15
	v_cndmask_b32_e32 v117, v229, v3, vcc
	v_or_b32_e32 v3, 0x7a0, v81
	v_sub_u32_e32 v3, v80, v3
	v_cmp_lt_i32_e32 vcc, -1, v3
	v_cvt_f32_u32_e32 v3, v3
	v_max3_f32 v2, v2, v116, v117
	v_fma_f32 v3, -v124, v3, v16
	v_cndmask_b32_e32 v125, v229, v3, vcc
	v_or_b32_e32 v3, 0x7b0, v81
	v_sub_u32_e32 v3, v80, v3
	v_cmp_lt_i32_e32 vcc, -1, v3
	v_cvt_f32_u32_e32 v3, v3
	s_and_b64 vcc, s[0:1], vcc
	v_add_u32_e32 v80, 64, v4
	v_fma_f32 v3, -v124, v3, v17
	v_cndmask_b32_e32 v81, v229, v3, vcc
	v_xor_b32_e32 v3, 32, v228
	v_cmp_lt_i32_e32 vcc, v3, v80
	v_max3_f32 v2, v2, v125, v81
	s_nop 0
	v_cndmask_b32_e32 v3, v228, v3, vcc
	v_lshlrev_b32_e32 v172, 2, v3
	ds_bpermute_b32 v3, v172, v2
	s_waitcnt lgkmcnt(0)
	v_max_f32_e32 v3, v3, v3
	v_max_f32_e32 v2, v2, v3
	v_cmp_neq_f32_e32 vcc, s5, v2
	s_nop 1
	v_cndmask_b32_e32 v126, 0, v2, vcc
	v_sub_f32_e32 v4, v52, v126
	v_sub_f32_e32 v52, v88, v126
	v_sub_f32_e32 v22, v38, v126
	v_sub_f32_e32 v38, v44, v126
	v_sub_f32_e32 v44, v82, v126
	v_exp_f32_e32 v82, v52
	v_sub_f32_e32 v52, v89, v126
	v_sub_f32_e32 v23, v39, v126
	v_sub_f32_e32 v39, v45, v126
	v_sub_f32_e32 v45, v83, v126
	v_exp_f32_e32 v83, v52
	v_sub_f32_e32 v52, v90, v126
	v_sub_f32_e32 v18, v34, v126
	v_sub_f32_e32 v34, v40, v126
	v_sub_f32_e32 v40, v46, v126
	v_sub_f32_e32 v46, v84, v126
	v_exp_f32_e32 v84, v52
	v_sub_f32_e32 v52, v91, v126
	v_sub_f32_e32 v19, v35, v126
	v_sub_f32_e32 v35, v41, v126
	v_sub_f32_e32 v41, v47, v126
	v_sub_f32_e32 v47, v85, v126
	v_exp_f32_e32 v85, v52
	v_sub_f32_e32 v52, v92, v126
	v_sub_f32_e32 v20, v36, v126
	v_sub_f32_e32 v36, v42, v126
	v_sub_f32_e32 v42, v48, v126
	v_sub_f32_e32 v48, v86, v126
	v_exp_f32_e32 v86, v52
	v_sub_f32_e32 v52, v93, v126
	v_sub_f32_e32 v21, v37, v126
	v_sub_f32_e32 v37, v43, v126
	v_sub_f32_e32 v43, v49, v126
	v_sub_f32_e32 v49, v87, v126
	v_exp_f32_e32 v87, v52
	v_sub_f32_e32 v52, v94, v126
	v_exp_f32_e32 v88, v52
	v_sub_f32_e32 v52, v95, v126
	v_exp_f32_e32 v89, v52
	v_sub_f32_e32 v52, v96, v126
	v_exp_f32_e32 v90, v52
	v_sub_f32_e32 v52, v97, v126
	v_exp_f32_e32 v91, v52
	v_sub_f32_e32 v52, v114, v126
	v_sub_f32_e32 v2, v66, v126
	v_exp_f32_e32 v92, v52
	v_sub_f32_e32 v52, v115, v126
	v_exp_f32_e32 v2, v2
	v_sub_f32_e32 v3, v67, v126
	v_exp_f32_e32 v93, v52
	v_sub_f32_e32 v52, v116, v126
	v_exp_f32_e32 v3, v3
	v_exp_f32_e32 v94, v52
	v_sub_f32_e32 v52, v117, v126
	v_exp_f32_e32 v4, v4
	v_sub_f32_e32 v5, v53, v126
	v_exp_f32_e32 v95, v52
	v_sub_f32_e32 v52, v125, v126
	v_exp_f32_e32 v5, v5
	v_sub_f32_e32 v6, v54, v126
	v_exp_f32_e32 v96, v52
	v_sub_f32_e32 v52, v81, v126
	v_exp_f32_e32 v6, v6
	v_sub_f32_e32 v7, v55, v126
	v_exp_f32_e32 v97, v52
	v_add_f32_e32 v52, 0, v2
	v_exp_f32_e32 v7, v7
	v_sub_f32_e32 v8, v56, v126
	v_add_f32_e32 v52, v3, v52
	v_exp_f32_e32 v8, v8
	v_sub_f32_e32 v9, v57, v126
	v_add_f32_e32 v52, v4, v52
	v_exp_f32_e32 v9, v9
	v_sub_f32_e32 v10, v58, v126
	v_add_f32_e32 v52, v5, v52
	v_exp_f32_e32 v10, v10
	v_sub_f32_e32 v11, v59, v126
	v_add_f32_e32 v52, v6, v52
	v_exp_f32_e32 v11, v11
	v_sub_f32_e32 v12, v60, v126
	v_add_f32_e32 v52, v7, v52
	v_exp_f32_e32 v12, v12
	v_sub_f32_e32 v13, v61, v126
	v_add_f32_e32 v52, v8, v52
	v_exp_f32_e32 v13, v13
	v_sub_f32_e32 v14, v62, v126
	v_add_f32_e32 v52, v9, v52
	v_exp_f32_e32 v14, v14
	v_sub_f32_e32 v15, v63, v126
	v_add_f32_e32 v52, v10, v52
	v_exp_f32_e32 v15, v15
	v_sub_f32_e32 v16, v64, v126
	v_add_f32_e32 v52, v11, v52
	v_exp_f32_e32 v16, v16
	v_sub_f32_e32 v17, v65, v126
	v_add_f32_e32 v52, v12, v52
	v_exp_f32_e32 v17, v17
	v_add_f32_e32 v52, v13, v52
	v_exp_f32_e32 v18, v18
	v_add_f32_e32 v52, v14, v52
	v_exp_f32_e32 v19, v19
	v_add_f32_e32 v52, v15, v52
	v_exp_f32_e32 v20, v20
	v_add_f32_e32 v52, v16, v52
; __device__ __forceinline__ void unit(LAS unsigned char* lds, const bf16* Z, const bf16* kct, const bf16* vct, bf16* OAp, int b, int g, int iq, const int tid_in) {
;     ...
;             for (int r = 0; r < 16; ++r) { const float e = __builtin_amdgcn_exp2f(p[blk][r] - msafe); p[blk][r] = e; l += e; }
;         l += __shfl_xor(l, 32);
;         const float inv = l > 0.f ? 1.0f / l : 0.f;
; #pragma unroll
;         for (int blk = 0; blk < 4; ++blk)
; #pragma unroll
;             for (int r = 0; r < 16; ++r) p[blk][r] *= inv;
; #pragma unroll
;         for (int blk = 0; blk < 4; ++blk)
; #pragma unroll
;             for (int rq = 0; rq < 4; ++rq) { const int n = 8 * blk + 2 * rq + hi;
;                 IA[(j * 64 + tl) * 32 + n] = 2.f * (p[blk][4 * rq] + p[blk][4 * rq + 1] + p[blk][4 * rq + 2]) + p[blk][4 * rq + 3];
;                 IB[(j * 64 + tl) * 32 + n] = p[blk][4 * rq + 3]; }
	v_exp_f32_e32 v21, v21
	v_add_f32_e32 v52, v17, v52
	v_exp_f32_e32 v22, v22
	v_add_f32_e32 v52, v18, v52
	v_exp_f32_e32 v23, v23
	v_add_f32_e32 v52, v19, v52
	v_exp_f32_e32 v34, v34
	v_add_f32_e32 v52, v20, v52
	v_exp_f32_e32 v35, v35
	v_add_f32_e32 v52, v21, v52
	v_exp_f32_e32 v36, v36
	v_add_f32_e32 v52, v22, v52
	v_exp_f32_e32 v37, v37
	v_add_f32_e32 v52, v23, v52
	v_exp_f32_e32 v38, v38
	v_add_f32_e32 v52, v34, v52
	v_exp_f32_e32 v39, v39
	v_add_f32_e32 v52, v35, v52
	v_exp_f32_e32 v40, v40
	v_add_f32_e32 v52, v36, v52
	v_exp_f32_e32 v41, v41
	v_add_f32_e32 v52, v37, v52
	v_exp_f32_e32 v42, v42
	v_add_f32_e32 v52, v38, v52
	v_exp_f32_e32 v43, v43
	v_add_f32_e32 v52, v39, v52
	v_exp_f32_e32 v44, v44
	v_add_f32_e32 v52, v40, v52
	v_exp_f32_e32 v45, v45
	v_add_f32_e32 v52, v41, v52
	v_exp_f32_e32 v46, v46
	v_add_f32_e32 v52, v42, v52
	v_exp_f32_e32 v47, v47
	v_add_f32_e32 v52, v43, v52
	v_exp_f32_e32 v48, v48
	v_add_f32_e32 v52, v44, v52
	v_exp_f32_e32 v49, v49
	v_sub_f32_e32 v24, v24, v126
	v_add_f32_e32 v52, v45, v52
	v_exp_f32_e32 v24, v24
	v_sub_f32_e32 v25, v25, v126
	v_add_f32_e32 v52, v46, v52
	v_exp_f32_e32 v25, v25
	v_sub_f32_e32 v26, v26, v126
	v_add_f32_e32 v52, v47, v52
	v_exp_f32_e32 v26, v26
	v_sub_f32_e32 v27, v27, v126
	v_add_f32_e32 v52, v48, v52
	v_exp_f32_e32 v27, v27
	v_sub_f32_e32 v28, v28, v126
	v_add_f32_e32 v52, v49, v52
	v_exp_f32_e32 v28, v28
	v_sub_f32_e32 v29, v29, v126
	v_add_f32_e32 v52, v24, v52
	v_exp_f32_e32 v29, v29
	v_sub_f32_e32 v30, v30, v126
	v_add_f32_e32 v52, v25, v52
	v_exp_f32_e32 v30, v30
	v_sub_f32_e32 v31, v31, v126
	v_add_f32_e32 v52, v26, v52
	v_exp_f32_e32 v31, v31
	v_sub_f32_e32 v32, v32, v126
	v_add_f32_e32 v52, v27, v52
	v_exp_f32_e32 v32, v32
	v_sub_f32_e32 v33, v33, v126
	v_add_f32_e32 v52, v28, v52
	v_exp_f32_e32 v33, v33
	v_add_f32_e32 v52, v29, v52
	v_add_f32_e32 v52, v30, v52
	v_add_f32_e32 v52, v31, v52
	v_add_f32_e32 v52, v32, v52
	v_add_f32_e32 v52, v33, v52
	v_add_f32_e32 v52, v82, v52
	v_add_f32_e32 v52, v83, v52
	v_add_f32_e32 v52, v84, v52
	v_add_f32_e32 v52, v85, v52
	v_add_f32_e32 v52, v86, v52
	v_add_f32_e32 v52, v87, v52
	v_add_f32_e32 v52, v88, v52
	v_add_f32_e32 v52, v89, v52
	v_add_f32_e32 v52, v90, v52
	v_add_f32_e32 v52, v91, v52
	v_add_f32_e32 v52, v92, v52
	v_add_f32_e32 v52, v93, v52
	v_add_f32_e32 v52, v94, v52
	v_add_f32_e32 v52, v95, v52
	v_add_f32_e32 v52, v96, v52
	v_add_f32_e32 v52, v97, v52
	ds_bpermute_b32 v53, v172, v52
	s_waitcnt lgkmcnt(0)
	v_add_f32_e32 v52, v52, v53
	v_div_scale_f32 v53, s[6:7], v52, v52, 1.0
	v_rcp_f32_e32 v54, v53
	v_cmp_lt_f32_e64 s[0:1], 0, v52
	v_fma_f32 v55, -v53, v54, 1.0
	v_fmac_f32_e32 v54, v55, v54
	v_div_scale_f32 v55, vcc, 1.0, v52, 1.0
	v_mul_f32_e32 v56, v55, v54
	v_fma_f32 v57, -v53, v56, v55
	v_fmac_f32_e32 v56, v57, v54
	v_fma_f32 v53, -v53, v56, v55
	v_div_fmas_f32 v53, v53, v54, v56
	v_div_fixup_f32 v52, v53, v52, 1.0
	v_cndmask_b32_e64 v114, 0, v52, s[0:1]
	v_pk_mul_f32 v[2:3], v[2:3], v[114:115] op_sel_hi:[1,0]
	v_pk_mul_f32 v[6:7], v[6:7], v[114:115] op_sel_hi:[1,0]
	v_pk_mul_f32 v[116:117], v[10:11], v[114:115] op_sel_hi:[1,0]
	s_lshl_b32 s0, s4, 11
	v_lshlrev_b32_e32 v10, 5, v68
	v_pk_mul_f32 v[4:5], v[4:5], v[114:115] op_sel_hi:[1,0]
	v_pk_mul_f32 v[8:9], v[8:9], v[114:115] op_sel_hi:[1,0]
	v_pk_mul_f32 v[126:127], v[12:13], v[114:115] op_sel_hi:[1,0]
	v_or3_b32 v10, v10, s0, v74
	v_lshlrev_b32_e32 v216, 5, v68
	v_or_b32_e32 v216, s0, v216
	v_lshl_add_u32 v216, v216, 2, 0
	v_add_u32_e32 v216, 0xd400, v216
	v_and_b32_e32 v217, 31, v68
	v_add_lshl_u32 v217, v217, v74, 2
	v_mov_b32_e32 v218, 0x7c
	v_add_f32_e32 v11, v2, v3
	v_add_f32_e32 v13, v6, v7
	v_add_f32_e32 v11, v4, v11
	v_lshl_add_u32 v10, v10, 2, 0
	v_add_f32_e32 v13, v8, v13
	v_pk_mul_f32 v[128:129], v[14:15], v[114:115] op_sel_hi:[1,0]
	v_fma_f32 v11, 2.0, v11, v5
	v_add_u32_e32 v12, 0x15400, v10
	v_fma_f32 v13, 2.0, v13, v9
	v_add_u32_e32 v10, 0xd400, v10
	v_pk_mul_f32 v[130:131], v[16:17], v[114:115] op_sel_hi:[1,0]
	v_add_u32_e32 v219, 0, v217
	v_add_u32_e32 v220, 8, v217
	v_and_or_b32 v219, v219, v218, v216
	v_and_or_b32 v220, v220, v218, v216
	ds_write_b32 v219, v11
	ds_write_b32 v219, v5 offset:32768
	ds_write_b32 v220, v13
	ds_write_b32 v220, v9 offset:32768
	v_add_f32_e32 v11, v116, v117
	v_add_f32_e32 v13, v128, v129
	v_add_f32_e32 v11, v126, v11
	v_add_f32_e32 v13, v130, v13
	v_pk_mul_f32 v[132:133], v[18:19], v[114:115] op_sel_hi:[1,0]
	v_pk_mul_f32 v[136:137], v[22:23], v[114:115] op_sel_hi:[1,0]
	v_fma_f32 v11, 2.0, v11, v127
	v_fma_f32 v13, 2.0, v13, v131
	v_pk_mul_f32 v[134:135], v[20:21], v[114:115] op_sel_hi:[1,0]
	v_pk_mul_f32 v[138:139], v[34:35], v[114:115] op_sel_hi:[1,0]
	v_add_u32_e32 v219, 16, v217
	v_add_u32_e32 v220, 24, v217
	v_and_or_b32 v219, v219, v218, v216
	v_and_or_b32 v220, v220, v218, v216
	ds_write_b32 v219, v11
	ds_write_b32 v219, v127 offset:32768
	ds_write_b32 v220, v13
	ds_write_b32 v220, v131 offset:32768
	v_add_f32_e32 v11, v132, v133
	v_add_f32_e32 v13, v136, v137
	v_add_f32_e32 v11, v134, v11
	v_add_f32_e32 v13, v138, v13
	v_pk_mul_f32 v[140:141], v[36:37], v[114:115] op_sel_hi:[1,0]
	v_pk_mul_f32 v[144:145], v[40:41], v[114:115] op_sel_hi:[1,0]
	v_fma_f32 v11, 2.0, v11, v135
	v_fma_f32 v13, 2.0, v13, v139
	v_pk_mul_f32 v[142:143], v[38:39], v[114:115] op_sel_hi:[1,0]
	v_pk_mul_f32 v[146:147], v[42:43], v[114:115] op_sel_hi:[1,0]
	v_add_u32_e32 v219, 32, v217
	v_add_u32_e32 v220, 40, v217
	v_and_or_b32 v219, v219, v218, v216
	v_and_or_b32 v220, v220, v218, v216
	ds_write_b32 v219, v11
	ds_write_b32 v219, v135 offset:32768
	ds_write_b32 v220, v13
	ds_write_b32 v220, v139 offset:32768
	v_add_f32_e32 v11, v140, v141
; #define LAS __attribute__((address_space(3)))
; __device__ __forceinline__ unsigned cvt_pk_bf16(float lo, float hi) { f32x2_t v = {lo, hi}; bf16x2_t b = __builtin_convertvector(v, bf16x2_t); return __builtin_bit_cast(unsigned, b); }
; #define MFMA32(a, b, c) __builtin_amdgcn_mfma_f32_32x32x16_bf16((a), (b), (c), 0, 0, 0)
; __device__ __forceinline__ void unit(LAS unsigned char* lds, const bf16* Z, const bf16* kct, const bf16* vct, bf16* OAp, int b, int g, int iq, const int tid_in) {
;     ...
;             for (int rq = 0; rq < 4; ++rq) { const int n = 8 * blk + 2 * rq + hi;
;                 IA[(j * 64 + tl) * 32 + n] = 2.f * (p[blk][4 * rq] + p[blk][4 * rq + 1] + p[blk][4 * rq + 2]) + p[blk][4 * rq + 3];
;                 IB[(j * 64 + tl) * 32 + n] = p[blk][4 * rq + 3]; }
;         f32x16 oc[2];
; #pragma unroll
;         for (int r = 0; r < 16; ++r) { oc[0][r] = 0.f; oc[1][r] = 0.f; }
; #pragma unroll
;         for (int s = 0; s < 8; ++s) { const int blk = s >> 1, rb = 8 * (s & 1);
;             u32x4 pw; pw.x = cvt_pk_bf16(p[blk][rb + 0], p[blk][rb + 1]); pw.y = cvt_pk_bf16(p[blk][rb + 2], p[blk][rb + 3]); pw.z = cvt_pk_bf16(p[blk][rb + 4], p[blk][rb + 5]); pw.w = cvt_pk_bf16(p[blk][rb + 6], p[blk][rb + 7]);
;             const bf16x8 pa = __builtin_bit_cast(bf16x8, pw);
; #pragma unroll
;             for (int db = 0; db < 2; ++db) { const bf16x8 vf = *(const LAS bf16x8*)(VC + (32 * db + r32) * VST2 + 16 * s + 8 * hi); oc[db] = MFMA32(vf, pa, oc[db]); } }
; #pragma unroll
;         for (int r = 0; r < 16; ++r) { otot[0][r] += gate[0] * oc[0][r]; otot[1][r] += gate[0] * oc[1][r]; }
;     }
;     __syncthreads();
;     {
;         const int n = lane & 31;
; #pragma unroll
;         for (int q = 0; q < 4; ++q) { const int tk = (tid >> 5) + 16 * q;
;             float imp = 0.f;
; #pragma unroll
;             for (int jj = 0; jj < 4; ++jj) { imp += IA[(jj * 64 + tk) * 32 + n]; if (n > 0) imp += IB[(jj * 64 + tk) * 32 + n - 1]; }
	v_add_f32_e32 v13, v144, v145
	v_add_f32_e32 v11, v142, v11
	v_add_f32_e32 v13, v146, v13
	v_pk_mul_f32 v[60:61], v[44:45], v[114:115] op_sel_hi:[1,0]
	v_pk_mul_f32 v[64:65], v[48:49], v[114:115] op_sel_hi:[1,0]
	v_fma_f32 v11, 2.0, v11, v143
	v_fma_f32 v13, 2.0, v13, v147
	v_pk_mul_f32 v[62:63], v[46:47], v[114:115] op_sel_hi:[1,0]
	v_pk_mul_f32 v[66:67], v[24:25], v[114:115] op_sel_hi:[1,0]
	v_add_u32_e32 v219, 48, v217
	v_add_u32_e32 v220, 56, v217
	v_and_or_b32 v219, v219, v218, v216
	v_and_or_b32 v220, v220, v218, v216
	ds_write_b32 v219, v11
	ds_write_b32 v219, v143 offset:32768
	ds_write_b32 v220, v13
	ds_write_b32 v220, v147 offset:32768
	v_add_f32_e32 v11, v60, v61
	v_add_f32_e32 v13, v64, v65
	v_add_f32_e32 v11, v62, v11
	v_add_f32_e32 v13, v66, v13
	v_pk_mul_f32 v[52:53], v[26:27], v[114:115] op_sel_hi:[1,0]
	v_pk_mul_f32 v[56:57], v[30:31], v[114:115] op_sel_hi:[1,0]
	v_fma_f32 v11, 2.0, v11, v63
	v_fma_f32 v13, 2.0, v13, v67
	v_pk_mul_f32 v[54:55], v[28:29], v[114:115] op_sel_hi:[1,0]
	v_pk_mul_f32 v[58:59], v[32:33], v[114:115] op_sel_hi:[1,0]
	v_add_u32_e32 v219, 64, v217
	v_add_u32_e32 v220, 72, v217
	v_and_or_b32 v219, v219, v218, v216
	v_and_or_b32 v220, v220, v218, v216
	ds_write_b32 v219, v11
	ds_write_b32 v219, v63 offset:32768
	ds_write_b32 v220, v13
	ds_write_b32 v220, v67 offset:32768
	v_add_f32_e32 v11, v52, v53
	v_add_f32_e32 v13, v56, v57
	v_add_f32_e32 v11, v54, v11
	v_add_f32_e32 v13, v58, v13
	v_pk_mul_f32 v[42:43], v[82:83], v[114:115] op_sel_hi:[1,0]
	v_pk_mul_f32 v[46:47], v[86:87], v[114:115] op_sel_hi:[1,0]
	v_fma_f32 v11, 2.0, v11, v55
	v_fma_f32 v13, 2.0, v13, v59
	v_pk_mul_f32 v[44:45], v[84:85], v[114:115] op_sel_hi:[1,0]
	v_pk_mul_f32 v[48:49], v[88:89], v[114:115] op_sel_hi:[1,0]
	v_add_u32_e32 v219, 80, v217
	v_add_u32_e32 v220, 88, v217
	v_and_or_b32 v219, v219, v218, v216
	v_and_or_b32 v220, v220, v218, v216
	ds_write_b32 v219, v11
	ds_write_b32 v219, v55 offset:32768
	ds_write_b32 v220, v13
	ds_write_b32 v220, v59 offset:32768
	v_add_f32_e32 v11, v42, v43
	v_add_f32_e32 v13, v46, v47
	v_add_f32_e32 v11, v44, v11
	v_add_f32_e32 v13, v48, v13
	v_pk_mul_f32 v[34:35], v[90:91], v[114:115] op_sel_hi:[1,0]
	v_pk_mul_f32 v[38:39], v[94:95], v[114:115] op_sel_hi:[1,0]
	v_fma_f32 v11, 2.0, v11, v45
	v_fma_f32 v13, 2.0, v13, v49
	v_pk_mul_f32 v[36:37], v[92:93], v[114:115] op_sel_hi:[1,0]
	v_pk_mul_f32 v[40:41], v[96:97], v[114:115] op_sel_hi:[1,0]
	v_add_u32_e32 v219, 96, v217
	v_add_u32_e32 v220, 104, v217
	v_and_or_b32 v219, v219, v218, v216
	v_and_or_b32 v220, v220, v218, v216
	ds_write_b32 v219, v11
	ds_write_b32 v219, v45 offset:32768
	ds_write_b32 v220, v13
	ds_write_b32 v220, v49 offset:32768
	v_add_f32_e32 v11, v34, v35
	v_add_f32_e32 v13, v38, v39
	v_add_f32_e32 v11, v36, v11
	v_add_f32_e32 v13, v40, v13
	v_fma_f32 v11, 2.0, v11, v37
	v_fma_f32 v13, 2.0, v13, v41
	s_movk_i32 s0, 0x110
	v_add_u32_e32 v219, 112, v217
	v_add_u32_e32 v220, 120, v217
	v_and_or_b32 v219, v219, v218, v216
	v_and_or_b32 v220, v220, v218, v216
	ds_write_b32 v219, v11
	ds_write_b32 v219, v37 offset:32768
	ds_write_b32 v220, v13
	ds_write_b32 v220, v41 offset:32768
	v_mad_u32_u24 v81, v73, s0, v76
	v_cvt_pk_bf16_f32 v2, v2, v3
	v_cvt_pk_bf16_f32 v3, v4, v5
	v_cvt_pk_bf16_f32 v4, v6, v7
	v_cvt_pk_bf16_f32 v5, v8, v9
	ds_read_b128 v[6:9], v81 offset:36864
	ds_read_b128 v[82:85], v81 offset:36896
	s_waitcnt lgkmcnt(1)
	v_mfma_f32_32x32x16_bf16 v[18:33], v[6:9], v[2:5], 0
	ds_read_b128 v[6:9], v81 offset:45568
	v_cvt_pk_bf16_f32 v86, v116, v117
	v_cvt_pk_bf16_f32 v87, v126, v127
	v_cvt_pk_bf16_f32 v88, v128, v129
	v_cvt_pk_bf16_f32 v89, v130, v131
	v_cvt_pk_bf16_f32 v60, v60, v61
	v_cvt_pk_bf16_f32 v61, v62, v63
	s_waitcnt lgkmcnt(1)
	v_mfma_f32_32x32x16_bf16 v[18:33], v[82:85], v[86:89], v[18:33]
	ds_read_b128 v[82:85], v81 offset:45600
	v_cvt_pk_bf16_f32 v62, v64, v65
	v_cvt_pk_bf16_f32 v63, v66, v67
	ds_read_b128 v[64:67], v81 offset:36992
	v_cvt_pk_bf16_f32 v52, v52, v53
	v_cvt_pk_bf16_f32 v53, v54, v55
	v_cvt_pk_bf16_f32 v54, v56, v57
	s_waitcnt lgkmcnt(2)
	v_mfma_f32_32x32x16_bf16 v[2:17], v[6:9], v[2:5], 0
	v_cvt_pk_bf16_f32 v55, v58, v59
	ds_read_b128 v[56:59], v81 offset:37024
	v_cvt_pk_bf16_f32 v42, v42, v43
	v_cvt_pk_bf16_f32 v43, v44, v45
	v_cvt_pk_bf16_f32 v44, v46, v47
	v_cvt_pk_bf16_f32 v45, v48, v49
	ds_read_b128 v[46:49], v81 offset:37056
	s_waitcnt lgkmcnt(3)
	v_mfma_f32_32x32x16_bf16 v[2:17], v[82:85], v[86:89], v[2:17]
	ds_read_b128 v[86:89], v81 offset:36928
	v_cvt_pk_bf16_f32 v82, v132, v133
	v_cvt_pk_bf16_f32 v83, v134, v135
	v_cvt_pk_bf16_f32 v84, v136, v137
	v_cvt_pk_bf16_f32 v85, v138, v139
	v_cvt_pk_bf16_f32 v34, v34, v35
	v_cvt_pk_bf16_f32 v35, v36, v37
	s_waitcnt lgkmcnt(0)
	v_mfma_f32_32x32x16_bf16 v[18:33], v[86:89], v[82:85], v[18:33]
	ds_read_b128 v[86:89], v81 offset:45632
	v_cvt_pk_bf16_f32 v36, v38, v39
	v_cvt_pk_bf16_f32 v37, v40, v41
	ds_read_b128 v[38:41], v81 offset:37088
	v_cmp_ne_u32_e64 s[0:1], 0, v73
	s_waitcnt lgkmcnt(1)
	v_mfma_f32_32x32x16_bf16 v[2:17], v[86:89], v[82:85], v[2:17]
	ds_read_b128 v[86:89], v81 offset:36960
	v_cvt_pk_bf16_f32 v82, v140, v141
	v_cvt_pk_bf16_f32 v83, v142, v143
	v_cvt_pk_bf16_f32 v84, v144, v145
	v_cvt_pk_bf16_f32 v85, v146, v147
	s_waitcnt lgkmcnt(0)
	s_nop 0
	v_mfma_f32_32x32x16_bf16 v[18:33], v[86:89], v[82:85], v[18:33]
	ds_read_b128 v[86:89], v81 offset:45664
	v_mfma_f32_32x32x16_bf16 v[18:33], v[64:67], v[60:63], v[18:33]
	ds_read_b128 v[64:67], v81 offset:45696
	s_waitcnt lgkmcnt(1)
	v_mfma_f32_32x32x16_bf16 v[2:17], v[86:89], v[82:85], v[2:17]
	v_mfma_f32_32x32x16_bf16 v[18:33], v[56:59], v[52:55], v[18:33]
	ds_read_b128 v[56:59], v81 offset:45728
	s_waitcnt lgkmcnt(1)
	v_mfma_f32_32x32x16_bf16 v[2:17], v[64:67], v[60:63], v[2:17]
	v_mfma_f32_32x32x16_bf16 v[18:33], v[46:49], v[42:45], v[18:33]
	ds_read_b128 v[46:49], v81 offset:45760
	s_waitcnt lgkmcnt(1)
	v_mfma_f32_32x32x16_bf16 v[2:17], v[56:59], v[52:55], v[2:17]
	v_mfma_f32_32x32x16_bf16 v[18:33], v[38:41], v[34:37], v[18:33]
	ds_read_b128 v[38:41], v81 offset:45792
	s_waitcnt lgkmcnt(0)
	s_barrier
	v_mfma_f32_32x32x16_bf16 v[2:17], v[46:49], v[42:45], v[2:17]
	v_mfma_f32_32x32x16_bf16 v[2:17], v[38:41], v[34:37], v[2:17]
	v_lshrrev_b32_e32 v216, 5, v78
	v_add_u32_e32 v217, v216, v73
	v_add_u32_e32 v218, -1, v217
	v_and_b32_e32 v217, 31, v217
	v_and_b32_e32 v218, 31, v218
	v_lshl_or_b32 v217, v216, 5, v217
	v_lshl_or_b32 v218, v216, 5, v218
	v_lshl_add_u32 v34, v217, 2, 0
	ds_read_b32 v35, v34 offset:54272
	v_lshlrev_b32_e32 v36, 2, v78
	s_waitcnt lgkmcnt(0)
	v_add_f32_e32 v35, 0, v35
	s_and_saveexec_b64 s[4:5], s[0:1]
	s_cbranch_execz .LBB0_418
	s_add_i32 s6, 0, 0x15400
	v_lshl_add_u32 v37, v218, 2, s6
	ds_read_b32 v37, v37
	s_waitcnt lgkmcnt(0)
	v_add_f32_e32 v35, v35, v37
; __device__ __forceinline__ void unit(LAS unsigned char* lds, const bf16* Z, const bf16* kct, const bf16* vct, bf16* OAp, int b, int g, int iq, const int tid_in) {
;     ...
;         for (int q = 0; q < 4; ++q) { const int tk = (tid >> 5) + 16 * q;
;             float imp = 0.f;
; #pragma unroll
;             for (int jj = 0; jj < 4; ++jj) { imp += IA[(jj * 64 + tk) * 32 + n]; if (n > 0) imp += IB[(jj * 64 + tk) * 32 + n - 1]; }
;             const bool valid = n <= iq, forced = (n == 0) || (n == iq) || (n == iq - 1);
;             const float sc = forced ? 1e4f : (valid ? imp : -1.0f);
;             int cnt = 0;
; #pragma unroll
;             for (int mm = 0; mm < 32; ++mm) { const float so = __shfl(sc, (lane & 32) + mm); cnt += (so > sc || (so == sc && mm < n)) ? 1 : 0; }
.LBB0_418:
	s_or_b64 exec, exec, s[4:5]
	ds_read_b32 v37, v34 offset:62464
	s_waitcnt lgkmcnt(0)
	v_add_f32_e32 v35, v35, v37
	s_and_saveexec_b64 s[4:5], s[0:1]
	s_cbranch_execz .LBB0_420
	s_add_i32 s6, 0, 0x15400
	v_lshl_add_u32 v37, v218, 2, s6
	ds_read_b32 v37, v37 offset:8192
	s_waitcnt lgkmcnt(0)
	v_add_f32_e32 v35, v35, v37
.LBB0_420:
	s_or_b64 exec, exec, s[4:5]
	v_add_u32_e32 v34, 0xd400, v34
	ds_read_b32 v37, v34 offset:16384
	s_waitcnt lgkmcnt(0)
	v_add_f32_e32 v35, v35, v37
	s_and_saveexec_b64 s[4:5], s[0:1]
	s_cbranch_execz .LBB0_422
	s_add_i32 s6, 0, 0x15400
	v_lshl_add_u32 v37, v218, 2, s6
	ds_read_b32 v37, v37 offset:16384
	s_waitcnt lgkmcnt(0)
	v_add_f32_e32 v35, v35, v37
.LBB0_422:
	s_or_b64 exec, exec, s[4:5]
	ds_read_b32 v34, v34 offset:24576
	s_waitcnt lgkmcnt(0)
	v_add_f32_e32 v35, v35, v34
	s_and_saveexec_b64 s[4:5], s[0:1]
	s_cbranch_execz .LBB0_424
	s_add_i32 s6, 0, 0x15400
	v_lshl_add_u32 v34, v218, 2, s6
	ds_read_b32 v34, v34 offset:24576
	s_waitcnt lgkmcnt(0)
	v_add_f32_e32 v35, v35, v34
.LBB0_424:
	s_or_b64 exec, exec, s[4:5]
	v_cmp_eq_u32_e32 vcc, s18, v73
	s_add_i32 s19, s18, -1
	v_cmp_lt_u32_e64 s[38:39], s18, v73
	s_or_b64 s[4:5], s[44:45], vcc
	v_cmp_eq_u32_e32 vcc, s19, v73
	v_and_b32_e32 v34, 32, v78
	s_or_b64 s[40:41], s[4:5], vcc
	v_and_or_b32 v39, v228, 64, v34
	v_cndmask_b32_e64 v35, v35, -1.0, s[38:39]
	v_cndmask_b32_e64 v38, v35, v230, s[40:41]
	v_lshlrev_b32_e32 v35, 2, v39
	ds_bpermute_b32 v39, v35, v38
	ds_bpermute_b32 v40, v35, v38 offset:8
	v_cmp_ne_u32_e64 s[56:57], 0, v73
	v_cmp_lt_u32_e64 s[92:93], 1, v73
	v_cmp_lt_u32_e64 s[50:51], 2, v73
	s_waitcnt lgkmcnt(1)
	v_cmp_lt_f32_e32 vcc, v38, v39
	v_cmp_eq_f32_e64 s[4:5], v38, v39
	ds_bpermute_b32 v39, v35, v38 offset:4
	s_and_b64 s[4:5], s[56:57], s[4:5]
	s_or_b64 vcc, vcc, s[4:5]
	v_cmp_lt_u32_e64 s[42:43], 3, v73
	ds_bpermute_b32 v41, v35, v38 offset:20
	s_waitcnt lgkmcnt(1)
	v_cmp_eq_f32_e64 s[6:7], v38, v39
	v_cmp_lt_f32_e64 s[4:5], v38, v39
	s_and_b64 s[6:7], s[6:7], s[92:93]
	s_or_b64 s[4:5], s[4:5], s[6:7]
	v_cmp_eq_f32_e64 s[6:7], v38, v40
	v_cndmask_b32_e64 v39, 0, 1, s[4:5]
	v_cmp_lt_f32_e64 s[4:5], v38, v40
	s_and_b64 s[6:7], s[6:7], s[50:51]
	s_or_b64 s[4:5], s[4:5], s[6:7]
	v_cndmask_b32_e64 v40, 0, 1, s[4:5]
	v_addc_co_u32_e32 v39, vcc, v40, v39, vcc
	ds_bpermute_b32 v40, v35, v38 offset:12
	v_cmp_lt_u32_e64 s[46:47], 4, v73
	v_cmp_lt_u32_e64 s[48:49], 5, v73
	v_cmp_lt_u32_e64 s[52:53], 6, v73
	v_cmp_lt_u32_e64 s[54:55], 7, v73
	s_waitcnt lgkmcnt(0)
	v_cmp_eq_f32_e64 s[4:5], v38, v40
	v_cmp_lt_f32_e32 vcc, v38, v40
	s_and_b64 s[4:5], s[4:5], s[42:43]
	s_or_b64 s[4:5], vcc, s[4:5]
	v_cndmask_b32_e64 v40, 0, 1, s[4:5]
	v_add_u32_e32 v39, v39, v40
	ds_bpermute_b32 v40, v35, v38 offset:16
	v_cmp_lt_u32_e64 s[58:59], 8, v73
	v_cmp_lt_u32_e64 s[60:61], 9, v73
	v_cmp_lt_u32_e64 s[62:63], 10, v73
	v_cmp_lt_u32_e64 s[64:65], 11, v73
	s_waitcnt lgkmcnt(0)
	v_cmp_eq_f32_e64 s[4:5], v38, v40
	v_cmp_lt_f32_e32 vcc, v38, v40
	s_and_b64 s[4:5], s[4:5], s[46:47]
	s_or_b64 s[4:5], vcc, s[4:5]
	v_cndmask_b32_e64 v40, 0, 1, s[4:5]
	v_cmp_eq_f32_e64 s[4:5], v38, v41
	v_cmp_lt_f32_e32 vcc, v38, v41
	s_and_b64 s[4:5], s[4:5], s[48:49]
	s_or_b64 s[4:5], vcc, s[4:5]
	v_cndmask_b32_e64 v41, 0, 1, s[4:5]
	v_add3_u32 v39, v39, v40, v41
	ds_bpermute_b32 v40, v35, v38 offset:24
	ds_bpermute_b32 v41, v35, v38 offset:28
	v_cmp_lt_u32_e64 s[68:69], 12, v73
	v_cmp_lt_u32_e64 s[70:71], 13, v73
	v_cmp_lt_u32_e64 s[72:73], 14, v73
	s_waitcnt lgkmcnt(1)
	v_cmp_eq_f32_e64 s[4:5], v38, v40
	v_cmp_lt_f32_e32 vcc, v38, v40
	s_and_b64 s[4:5], s[4:5], s[52:53]
	s_or_b64 s[4:5], vcc, s[4:5]
	v_cndmask_b32_e64 v40, 0, 1, s[4:5]
	s_waitcnt lgkmcnt(0)
	v_cmp_eq_f32_e64 s[4:5], v38, v41
	v_cmp_lt_f32_e32 vcc, v38, v41
	s_and_b64 s[4:5], s[4:5], s[54:55]
	s_or_b64 s[4:5], vcc, s[4:5]
	v_cndmask_b32_e64 v41, 0, 1, s[4:5]
	v_add3_u32 v39, v39, v40, v41
	ds_bpermute_b32 v40, v35, v38 offset:32
	ds_bpermute_b32 v41, v35, v38 offset:36
	v_cmp_lt_u32_e64 s[74:75], 15, v73
	v_cmp_lt_u32_e64 s[76:77], 16, v73
	v_cmp_lt_u32_e64 s[78:79], 17, v73
	s_waitcnt lgkmcnt(1)
	v_cmp_eq_f32_e64 s[4:5], v38, v40
	v_cmp_lt_f32_e32 vcc, v38, v40
	s_and_b64 s[4:5], s[4:5], s[58:59]
	s_or_b64 s[4:5], vcc, s[4:5]
	v_cndmask_b32_e64 v40, 0, 1, s[4:5]
	s_waitcnt lgkmcnt(0)
	v_cmp_eq_f32_e64 s[4:5], v38, v41
	v_cmp_lt_f32_e32 vcc, v38, v41
	s_and_b64 s[4:5], s[4:5], s[60:61]
	s_or_b64 s[4:5], vcc, s[4:5]
	v_cndmask_b32_e64 v41, 0, 1, s[4:5]
	v_add3_u32 v39, v39, v40, v41
	ds_bpermute_b32 v40, v35, v38 offset:40
	ds_bpermute_b32 v41, v35, v38 offset:44
	v_cmp_lt_u32_e64 s[80:81], 18, v73
	v_cmp_lt_u32_e64 s[82:83], 19, v73
	v_cmp_lt_u32_e64 s[84:85], 20, v73
	s_waitcnt lgkmcnt(1)
	v_cmp_eq_f32_e64 s[4:5], v38, v40
	v_cmp_lt_f32_e32 vcc, v38, v40
	s_and_b64 s[4:5], s[4:5], s[62:63]
	s_or_b64 s[4:5], vcc, s[4:5]
	v_cndmask_b32_e64 v40, 0, 1, s[4:5]
	s_waitcnt lgkmcnt(0)
	v_cmp_eq_f32_e64 s[4:5], v38, v41
	v_cmp_lt_f32_e32 vcc, v38, v41
	s_and_b64 s[4:5], s[4:5], s[64:65]
	s_or_b64 s[4:5], vcc, s[4:5]
	v_cndmask_b32_e64 v41, 0, 1, s[4:5]
	v_add3_u32 v39, v39, v40, v41
	ds_bpermute_b32 v40, v35, v38 offset:48
	ds_bpermute_b32 v41, v35, v38 offset:52
	v_cmp_lt_u32_e64 s[86:87], 21, v73
	v_cmp_lt_u32_e64 s[88:89], 22, v73
	v_cmp_lt_u32_e64 s[90:91], 23, v73
	s_waitcnt lgkmcnt(1)
	v_cmp_eq_f32_e64 s[4:5], v38, v40
	v_cmp_lt_f32_e32 vcc, v38, v40
	s_and_b64 s[4:5], s[4:5], s[68:69]
	s_or_b64 s[4:5], vcc, s[4:5]
	v_cndmask_b32_e64 v40, 0, 1, s[4:5]
	s_waitcnt lgkmcnt(0)
; __device__ __forceinline__ void unit(LAS unsigned char* lds, const bf16* Z, const bf16* kct, const bf16* vct, bf16* OAp, int b, int g, int iq, const int tid_in) {
;     ...
;             for (int jj = 0; jj < 4; ++jj) { imp += IA[(jj * 64 + tk) * 32 + n]; if (n > 0) imp += IB[(jj * 64 + tk) * 32 + n - 1]; }
;             const bool valid = n <= iq, forced = (n == 0) || (n == iq) || (n == iq - 1);
;             const float sc = forced ? 1e4f : (valid ? imp : -1.0f);
;             int cnt = 0;
; #pragma unroll
;             for (int mm = 0; mm < 32; ++mm) { const float so = __shfl(sc, (lane & 32) + mm); cnt += (so > sc || (so == sc && mm < n)) ? 1 : 0; }
;             const unsigned long long bal = __ballot(cnt < 16);
;             if (n == 0) MSK[tk] = (unsigned)((lane & 32) ? (bal >> 32) : bal); }
	v_cmp_eq_f32_e64 s[4:5], v38, v41
	v_cmp_lt_f32_e32 vcc, v38, v41
	s_and_b64 s[4:5], s[4:5], s[70:71]
	s_or_b64 s[4:5], vcc, s[4:5]
	v_cndmask_b32_e64 v41, 0, 1, s[4:5]
	v_add3_u32 v39, v39, v40, v41
	ds_bpermute_b32 v40, v35, v38 offset:56
	ds_bpermute_b32 v41, v35, v38 offset:60
	v_cmp_lt_u32_e64 s[94:95], 24, v73
	v_cmp_lt_u32_e64 s[96:97], 25, v73
	v_cmp_lt_u32_e64 s[6:7], 26, v73
	s_waitcnt lgkmcnt(1)
	v_cmp_eq_f32_e64 s[4:5], v38, v40
	v_cmp_lt_f32_e32 vcc, v38, v40
	s_and_b64 s[4:5], s[4:5], s[72:73]
	s_or_b64 s[4:5], vcc, s[4:5]
	v_cndmask_b32_e64 v40, 0, 1, s[4:5]
	s_waitcnt lgkmcnt(0)
	v_cmp_eq_f32_e64 s[4:5], v38, v41
	v_cmp_lt_f32_e32 vcc, v38, v41
	s_and_b64 s[4:5], s[4:5], s[74:75]
	s_or_b64 s[4:5], vcc, s[4:5]
	v_cndmask_b32_e64 v41, 0, 1, s[4:5]
	v_add3_u32 v39, v39, v40, v41
	ds_bpermute_b32 v40, v35, v38 offset:64
	ds_bpermute_b32 v41, v35, v38 offset:68
	v_cmp_lt_u32_e64 s[10:11], 28, v73
	v_ashrrev_i32_e32 v37, 5, v78
	s_waitcnt lgkmcnt(1)
	v_cmp_eq_f32_e64 s[4:5], v38, v40
	v_cmp_lt_f32_e32 vcc, v38, v40
	s_and_b64 s[4:5], s[4:5], s[76:77]
	s_or_b64 s[4:5], vcc, s[4:5]
	v_cndmask_b32_e64 v40, 0, 1, s[4:5]
	s_waitcnt lgkmcnt(0)
	v_cmp_eq_f32_e64 s[4:5], v38, v41
	v_cmp_lt_f32_e32 vcc, v38, v41
	s_and_b64 s[4:5], s[4:5], s[78:79]
	s_or_b64 s[4:5], vcc, s[4:5]
	v_cndmask_b32_e64 v41, 0, 1, s[4:5]
	v_add3_u32 v39, v39, v40, v41
	ds_bpermute_b32 v40, v35, v38 offset:72
	ds_bpermute_b32 v41, v35, v38 offset:76
	s_waitcnt lgkmcnt(1)
	v_cmp_eq_f32_e64 s[4:5], v38, v40
	v_cmp_lt_f32_e32 vcc, v38, v40
	s_and_b64 s[4:5], s[4:5], s[80:81]
	s_or_b64 s[4:5], vcc, s[4:5]
	v_cndmask_b32_e64 v40, 0, 1, s[4:5]
	s_waitcnt lgkmcnt(0)
	v_cmp_eq_f32_e64 s[4:5], v38, v41
	v_cmp_lt_f32_e32 vcc, v38, v41
	s_and_b64 s[4:5], s[4:5], s[82:83]
	s_or_b64 s[4:5], vcc, s[4:5]
	v_cndmask_b32_e64 v41, 0, 1, s[4:5]
	v_add3_u32 v39, v39, v40, v41
	ds_bpermute_b32 v40, v35, v38 offset:80
	ds_bpermute_b32 v41, v35, v38 offset:84
	s_waitcnt lgkmcnt(1)
	v_cmp_eq_f32_e64 s[4:5], v38, v40
	v_cmp_lt_f32_e32 vcc, v38, v40
	s_and_b64 s[4:5], s[4:5], s[84:85]
	s_or_b64 s[4:5], vcc, s[4:5]
	v_cndmask_b32_e64 v40, 0, 1, s[4:5]
	s_waitcnt lgkmcnt(0)
	v_cmp_eq_f32_e64 s[4:5], v38, v41
	v_cmp_lt_f32_e32 vcc, v38, v41
	s_and_b64 s[4:5], s[4:5], s[86:87]
	s_or_b64 s[4:5], vcc, s[4:5]
	v_cndmask_b32_e64 v41, 0, 1, s[4:5]
	v_add3_u32 v39, v39, v40, v41
	ds_bpermute_b32 v40, v35, v38 offset:88
	ds_bpermute_b32 v41, v35, v38 offset:92
	s_waitcnt lgkmcnt(1)
	v_cmp_eq_f32_e64 s[4:5], v38, v40
	v_cmp_lt_f32_e32 vcc, v38, v40
	s_and_b64 s[4:5], s[4:5], s[88:89]
	s_or_b64 s[4:5], vcc, s[4:5]
	v_cndmask_b32_e64 v40, 0, 1, s[4:5]
	s_waitcnt lgkmcnt(0)
	v_cmp_eq_f32_e64 s[4:5], v38, v41
	v_cmp_lt_f32_e32 vcc, v38, v41
	s_and_b64 s[4:5], s[4:5], s[90:91]
	s_or_b64 s[4:5], vcc, s[4:5]
	v_cndmask_b32_e64 v41, 0, 1, s[4:5]
	v_add3_u32 v39, v39, v40, v41
	ds_bpermute_b32 v40, v35, v38 offset:96
	ds_bpermute_b32 v41, v35, v38 offset:100
	s_waitcnt lgkmcnt(1)
	v_cmp_eq_f32_e64 s[4:5], v38, v40
	v_cmp_lt_f32_e32 vcc, v38, v40
	s_and_b64 s[4:5], s[4:5], s[94:95]
	s_or_b64 s[4:5], vcc, s[4:5]
	v_cndmask_b32_e64 v40, 0, 1, s[4:5]
	s_waitcnt lgkmcnt(0)
	v_cmp_eq_f32_e64 s[4:5], v38, v41
	v_cmp_lt_f32_e32 vcc, v38, v41
	s_and_b64 s[4:5], s[4:5], s[96:97]
	s_or_b64 s[4:5], vcc, s[4:5]
	v_cndmask_b32_e64 v41, 0, 1, s[4:5]
	v_add3_u32 v39, v39, v40, v41
	ds_bpermute_b32 v40, v35, v38 offset:104
	ds_bpermute_b32 v41, v35, v38 offset:108
	s_waitcnt lgkmcnt(1)
	v_cmp_eq_f32_e64 s[4:5], v38, v40
	v_cmp_lt_f32_e32 vcc, v38, v40
	s_and_b64 s[4:5], s[4:5], s[6:7]
	s_or_b64 s[4:5], vcc, s[4:5]
	v_cndmask_b32_e64 v40, 0, 1, s[4:5]
	s_waitcnt lgkmcnt(0)
	v_cmp_eq_f32_e64 s[8:9], v38, v41
	v_cmp_lt_u32_e64 s[4:5], 27, v73
	v_cmp_lt_f32_e32 vcc, v38, v41
	s_and_b64 s[8:9], s[8:9], s[4:5]
	s_or_b64 s[8:9], vcc, s[8:9]
	v_cndmask_b32_e64 v41, 0, 1, s[8:9]
	v_add3_u32 v39, v39, v40, v41
	ds_bpermute_b32 v40, v35, v38 offset:112
	ds_bpermute_b32 v41, v35, v38 offset:116
	s_waitcnt lgkmcnt(1)
	v_cmp_eq_f32_e64 s[8:9], v38, v40
	v_cmp_lt_f32_e32 vcc, v38, v40
	s_and_b64 s[8:9], s[8:9], s[10:11]
	s_or_b64 s[8:9], vcc, s[8:9]
	v_cndmask_b32_e64 v40, 0, 1, s[8:9]
	s_waitcnt lgkmcnt(0)
	v_cmp_eq_f32_e64 s[66:67], v38, v41
	v_cmp_lt_u32_e64 s[8:9], 29, v73
	v_cmp_lt_f32_e32 vcc, v38, v41
	s_and_b64 s[12:13], s[66:67], s[8:9]
	s_or_b64 s[12:13], vcc, s[12:13]
	v_cndmask_b32_e64 v41, 0, 1, s[12:13]
	v_add3_u32 v39, v39, v40, v41
	ds_bpermute_b32 v40, v35, v38 offset:120
	v_cmp_eq_u32_e64 s[66:67], 31, v73
	s_waitcnt lgkmcnt(0)
	v_cmp_lt_f32_e64 s[12:13], v38, v40
	v_cmp_eq_f32_e32 vcc, v38, v40
	ds_bpermute_b32 v40, v35, v38 offset:124
	s_and_b64 vcc, s[66:67], vcc
	s_or_b64 vcc, s[12:13], vcc
	s_waitcnt lgkmcnt(0)
	v_cmp_lt_f32_e64 s[12:13], v38, v40
	s_nop 1
	v_cndmask_b32_e64 v38, 0, 1, s[12:13]
	v_addc_co_u32_e32 v38, vcc, v39, v38, vcc
	v_cmp_gt_u32_e32 vcc, 16, v38
	s_and_saveexec_b64 s[12:13], s[44:45]
	s_nop 0
	v_lshrrev_b64 v[38:39], v34, vcc
	v_lshl_add_u32 v39, v37, 2, 0
	v_add_u32_e32 v39, 0x1d400, v39
	ds_write_b32 v39, v38
	s_or_b64 exec, exec, s[12:13]
	v_add_u32_e32 v84, 16, v37
	v_lshl_or_b32 v38, v84, 5, v73
	v_add_u32_e32 v217, v84, v73
	v_add_u32_e32 v218, -1, v217
	v_and_b32_e32 v217, 31, v217
	v_and_b32_e32 v218, 31, v218
	v_lshl_or_b32 v217, v84, 5, v217
	v_lshl_or_b32 v218, v84, 5, v218
	v_lshl_add_u32 v39, v217, 2, 0
	ds_read_b32 v40, v39 offset:54272
	s_waitcnt lgkmcnt(0)
	v_add_f32_e32 v40, 0, v40
	s_and_saveexec_b64 s[12:13], s[0:1]
	s_cbranch_execz .LBB0_428
	v_lshlrev_b32_e32 v41, 2, v38
	s_add_i32 s14, 0, 0x15400
	v_lshl_add_u32 v41, v218, 2, s14
	ds_read_b32 v41, v41
	s_waitcnt lgkmcnt(0)
	v_add_f32_e32 v40, v40, v41
; __device__ __forceinline__ void unit(LAS unsigned char* lds, const bf16* Z, const bf16* kct, const bf16* vct, bf16* OAp, int b, int g, int iq, const int tid_in) {
;     ...
;         for (int q = 0; q < 4; ++q) { const int tk = (tid >> 5) + 16 * q;
;             float imp = 0.f;
; #pragma unroll
;             for (int jj = 0; jj < 4; ++jj) { imp += IA[(jj * 64 + tk) * 32 + n]; if (n > 0) imp += IB[(jj * 64 + tk) * 32 + n - 1]; }
;             const bool valid = n <= iq, forced = (n == 0) || (n == iq) || (n == iq - 1);
;             const float sc = forced ? 1e4f : (valid ? imp : -1.0f);
;             int cnt = 0;
; #pragma unroll
;             for (int mm = 0; mm < 32; ++mm) { const float so = __shfl(sc, (lane & 32) + mm); cnt += (so > sc || (so == sc && mm < n)) ? 1 : 0; }
.LBB0_428:
	s_or_b64 exec, exec, s[12:13]
	ds_read_b32 v41, v39 offset:62464
	s_waitcnt lgkmcnt(0)
	v_add_f32_e32 v40, v40, v41
	s_and_saveexec_b64 s[12:13], s[0:1]
	s_cbranch_execz .LBB0_430
	s_add_i32 s14, 0, 0x15400
	v_lshl_add_u32 v41, v218, 2, s14
	ds_read_b32 v41, v41 offset:8192
	s_waitcnt lgkmcnt(0)
	v_add_f32_e32 v40, v40, v41
.LBB0_430:
	s_or_b64 exec, exec, s[12:13]
	v_add_u32_e32 v39, 0xd400, v39
	ds_read_b32 v41, v39 offset:16384
	s_waitcnt lgkmcnt(0)
	v_add_f32_e32 v40, v40, v41
	s_and_saveexec_b64 s[12:13], s[0:1]
	s_cbranch_execz .LBB0_432
	s_add_i32 s14, 0, 0x15400
	v_lshl_add_u32 v41, v218, 2, s14
	ds_read_b32 v41, v41 offset:16384
	s_waitcnt lgkmcnt(0)
	v_add_f32_e32 v40, v40, v41
.LBB0_432:
	s_or_b64 exec, exec, s[12:13]
	ds_read_b32 v39, v39 offset:24576
	s_waitcnt lgkmcnt(0)
	v_add_f32_e32 v85, v40, v39
	s_and_saveexec_b64 s[12:13], s[0:1]
	s_cbranch_execz .LBB0_434
	s_add_i32 s14, 0, 0x15400
	v_lshl_add_u32 v38, v218, 2, s14
	ds_read_b32 v38, v38 offset:24576
	s_waitcnt lgkmcnt(0)
	v_add_f32_e32 v85, v85, v38
.LBB0_434:
	s_or_b64 exec, exec, s[12:13]
	v_cndmask_b32_e64 v85, v85, -1.0, s[38:39]
	v_cndmask_b32_e64 v85, v85, v230, s[40:41]
	ds_bpermute_b32 v86, v35, v85
	v_or_b32_e32 v83, 4, v35
	ds_bpermute_b32 v87, v83, v85
	v_or_b32_e32 v82, 8, v35
	ds_bpermute_b32 v88, v82, v85
	s_waitcnt lgkmcnt(2)
	v_cmp_eq_f32_e64 s[12:13], v85, v86
	v_cmp_lt_f32_e32 vcc, v85, v86
	s_and_b64 s[12:13], s[56:57], s[12:13]
	s_or_b64 s[12:13], vcc, s[12:13]
	v_cndmask_b32_e64 v86, 0, 1, s[12:13]
	s_waitcnt lgkmcnt(1)
	v_cmp_eq_f32_e64 s[12:13], v85, v87
	v_cmp_lt_f32_e32 vcc, v85, v87
	s_and_b64 s[12:13], s[12:13], s[92:93]
	s_or_b64 s[12:13], vcc, s[12:13]
	v_cndmask_b32_e64 v87, 0, 1, s[12:13]
	s_waitcnt lgkmcnt(0)
	v_cmp_eq_f32_e64 s[12:13], v85, v88
	v_cmp_lt_f32_e32 vcc, v85, v88
	s_and_b64 s[12:13], s[12:13], s[50:51]
	s_or_b64 s[12:13], vcc, s[12:13]
	v_or_b32_e32 v81, 12, v35
	v_cndmask_b32_e64 v88, 0, 1, s[12:13]
	v_add3_u32 v86, v86, v87, v88
	ds_bpermute_b32 v87, v81, v85
	v_or_b32_e32 v67, 16, v35
	ds_bpermute_b32 v88, v67, v85
	v_or_b32_e32 v66, 20, v35
	v_or_b32_e32 v65, 24, v35
	s_waitcnt lgkmcnt(1)
	v_cmp_eq_f32_e64 s[12:13], v85, v87
	v_cmp_lt_f32_e32 vcc, v85, v87
	s_and_b64 s[12:13], s[12:13], s[42:43]
	s_or_b64 s[12:13], vcc, s[12:13]
	v_cndmask_b32_e64 v87, 0, 1, s[12:13]
	s_waitcnt lgkmcnt(0)
	v_cmp_eq_f32_e64 s[12:13], v85, v88
	v_cmp_lt_f32_e32 vcc, v85, v88
	s_and_b64 s[12:13], s[12:13], s[46:47]
	s_or_b64 s[12:13], vcc, s[12:13]
	v_cndmask_b32_e64 v88, 0, 1, s[12:13]
	v_add3_u32 v86, v86, v87, v88
	ds_bpermute_b32 v87, v66, v85
	ds_bpermute_b32 v88, v65, v85
	v_or_b32_e32 v64, 28, v35
	v_or_b32_e32 v63, 32, v35
	v_or_b32_e32 v62, 36, v35
	s_waitcnt lgkmcnt(1)
	v_cmp_eq_f32_e64 s[12:13], v85, v87
	v_cmp_lt_f32_e32 vcc, v85, v87
	s_and_b64 s[12:13], s[12:13], s[48:49]
	s_or_b64 s[12:13], vcc, s[12:13]
	v_cndmask_b32_e64 v87, 0, 1, s[12:13]
	s_waitcnt lgkmcnt(0)
	v_cmp_eq_f32_e64 s[12:13], v85, v88
	v_cmp_lt_f32_e32 vcc, v85, v88
	s_and_b64 s[12:13], s[12:13], s[52:53]
	s_or_b64 s[12:13], vcc, s[12:13]
	v_cndmask_b32_e64 v88, 0, 1, s[12:13]
	v_add3_u32 v86, v86, v87, v88
	ds_bpermute_b32 v87, v64, v85
	ds_bpermute_b32 v88, v63, v85
	v_or_b32_e32 v61, 40, v35
	v_or_b32_e32 v60, 44, v35
	v_or_b32_e32 v59, 48, v35
	s_waitcnt lgkmcnt(1)
	v_cmp_eq_f32_e64 s[12:13], v85, v87
	v_cmp_lt_f32_e32 vcc, v85, v87
	s_and_b64 s[12:13], s[12:13], s[54:55]
	s_or_b64 s[12:13], vcc, s[12:13]
	v_cndmask_b32_e64 v87, 0, 1, s[12:13]
	s_waitcnt lgkmcnt(0)
	v_cmp_eq_f32_e64 s[12:13], v85, v88
	v_cmp_lt_f32_e32 vcc, v85, v88
	s_and_b64 s[12:13], s[12:13], s[58:59]
	s_or_b64 s[12:13], vcc, s[12:13]
	v_cndmask_b32_e64 v88, 0, 1, s[12:13]
	v_add3_u32 v86, v86, v87, v88
	ds_bpermute_b32 v87, v62, v85
	ds_bpermute_b32 v88, v61, v85
	v_or_b32_e32 v58, 52, v35
	v_or_b32_e32 v57, 56, v35
	v_or_b32_e32 v56, 60, v35
	s_waitcnt lgkmcnt(1)
	v_cmp_eq_f32_e64 s[12:13], v85, v87
	v_cmp_lt_f32_e32 vcc, v85, v87
	s_and_b64 s[12:13], s[12:13], s[60:61]
	s_or_b64 s[12:13], vcc, s[12:13]
	v_cndmask_b32_e64 v87, 0, 1, s[12:13]
	s_waitcnt lgkmcnt(0)
	v_cmp_eq_f32_e64 s[12:13], v85, v88
	v_cmp_lt_f32_e32 vcc, v85, v88
	s_and_b64 s[12:13], s[12:13], s[62:63]
	s_or_b64 s[12:13], vcc, s[12:13]
	v_cndmask_b32_e64 v88, 0, 1, s[12:13]
	v_add3_u32 v86, v86, v87, v88
	ds_bpermute_b32 v87, v60, v85
	ds_bpermute_b32 v88, v59, v85
	v_or_b32_e32 v55, 64, v35
	v_or_b32_e32 v54, 0x44, v35
	v_or_b32_e32 v53, 0x48, v35
	s_waitcnt lgkmcnt(1)
	v_cmp_eq_f32_e64 s[12:13], v85, v87
	v_cmp_lt_f32_e32 vcc, v85, v87
	s_and_b64 s[12:13], s[12:13], s[64:65]
	s_or_b64 s[12:13], vcc, s[12:13]
	v_cndmask_b32_e64 v87, 0, 1, s[12:13]
	s_waitcnt lgkmcnt(0)
	v_cmp_eq_f32_e64 s[12:13], v85, v88
	v_cmp_lt_f32_e32 vcc, v85, v88
	s_and_b64 s[12:13], s[12:13], s[68:69]
	s_or_b64 s[12:13], vcc, s[12:13]
	v_cndmask_b32_e64 v88, 0, 1, s[12:13]
	v_add3_u32 v86, v86, v87, v88
	ds_bpermute_b32 v87, v58, v85
	ds_bpermute_b32 v88, v57, v85
	v_or_b32_e32 v52, 0x4c, v35
	v_or_b32_e32 v49, 0x50, v35
	v_or_b32_e32 v48, 0x54, v35
	s_waitcnt lgkmcnt(1)
	v_cmp_eq_f32_e64 s[12:13], v85, v87
	v_cmp_lt_f32_e32 vcc, v85, v87
	s_and_b64 s[12:13], s[12:13], s[70:71]
	s_or_b64 s[12:13], vcc, s[12:13]
	v_cndmask_b32_e64 v87, 0, 1, s[12:13]
	s_waitcnt lgkmcnt(0)
	v_cmp_eq_f32_e64 s[12:13], v85, v88
	v_cmp_lt_f32_e32 vcc, v85, v88
	s_and_b64 s[12:13], s[12:13], s[72:73]
	s_or_b64 s[12:13], vcc, s[12:13]
	v_cndmask_b32_e64 v88, 0, 1, s[12:13]
	v_add3_u32 v86, v86, v87, v88
	ds_bpermute_b32 v87, v56, v85
	ds_bpermute_b32 v88, v55, v85
	v_or_b32_e32 v47, 0x58, v35
	v_or_b32_e32 v46, 0x5c, v35
	v_or_b32_e32 v45, 0x60, v35
	s_waitcnt lgkmcnt(1)
; __device__ __forceinline__ void unit(LAS unsigned char* lds, const bf16* Z, const bf16* kct, const bf16* vct, bf16* OAp, int b, int g, int iq, const int tid_in) {
;     ...
;         for (int q = 0; q < 4; ++q) { const int tk = (tid >> 5) + 16 * q;
;             float imp = 0.f;
; #pragma unroll
;             for (int jj = 0; jj < 4; ++jj) { imp += IA[(jj * 64 + tk) * 32 + n]; if (n > 0) imp += IB[(jj * 64 + tk) * 32 + n - 1]; }
;             const bool valid = n <= iq, forced = (n == 0) || (n == iq) || (n == iq - 1);
;             const float sc = forced ? 1e4f : (valid ? imp : -1.0f);
;             int cnt = 0;
; #pragma unroll
;             for (int mm = 0; mm < 32; ++mm) { const float so = __shfl(sc, (lane & 32) + mm); cnt += (so > sc || (so == sc && mm < n)) ? 1 : 0; }
;             const unsigned long long bal = __ballot(cnt < 16);
;             if (n == 0) MSK[tk] = (unsigned)((lane & 32) ? (bal >> 32) : bal); }
	v_cmp_eq_f32_e64 s[12:13], v85, v87
	v_cmp_lt_f32_e32 vcc, v85, v87
	s_and_b64 s[12:13], s[12:13], s[74:75]
	s_or_b64 s[12:13], vcc, s[12:13]
	v_cndmask_b32_e64 v87, 0, 1, s[12:13]
	s_waitcnt lgkmcnt(0)
	v_cmp_eq_f32_e64 s[12:13], v85, v88
	v_cmp_lt_f32_e32 vcc, v85, v88
	s_and_b64 s[12:13], s[12:13], s[76:77]
	s_or_b64 s[12:13], vcc, s[12:13]
	v_cndmask_b32_e64 v88, 0, 1, s[12:13]
	v_add3_u32 v86, v86, v87, v88
	ds_bpermute_b32 v87, v54, v85
	ds_bpermute_b32 v88, v53, v85
	v_or_b32_e32 v44, 0x64, v35
	v_or_b32_e32 v43, 0x68, v35
	v_or_b32_e32 v42, 0x6c, v35
	s_waitcnt lgkmcnt(1)
	v_cmp_eq_f32_e64 s[12:13], v85, v87
	v_cmp_lt_f32_e32 vcc, v85, v87
	s_and_b64 s[12:13], s[12:13], s[78:79]
	s_or_b64 s[12:13], vcc, s[12:13]
	v_cndmask_b32_e64 v87, 0, 1, s[12:13]
	s_waitcnt lgkmcnt(0)
	v_cmp_eq_f32_e64 s[12:13], v85, v88
	v_cmp_lt_f32_e32 vcc, v85, v88
	s_and_b64 s[12:13], s[12:13], s[80:81]
	s_or_b64 s[12:13], vcc, s[12:13]
	v_cndmask_b32_e64 v88, 0, 1, s[12:13]
	v_add3_u32 v86, v86, v87, v88
	ds_bpermute_b32 v87, v52, v85
	ds_bpermute_b32 v88, v49, v85
	v_or_b32_e32 v41, 0x70, v35
	v_or_b32_e32 v40, 0x74, v35
	v_or_b32_e32 v39, 0x78, v35
	s_waitcnt lgkmcnt(1)
	v_cmp_eq_f32_e64 s[12:13], v85, v87
	v_cmp_lt_f32_e32 vcc, v85, v87
	s_and_b64 s[12:13], s[12:13], s[82:83]
	s_or_b64 s[12:13], vcc, s[12:13]
	v_cndmask_b32_e64 v87, 0, 1, s[12:13]
	s_waitcnt lgkmcnt(0)
	v_cmp_eq_f32_e64 s[12:13], v85, v88
	v_cmp_lt_f32_e32 vcc, v85, v88
	s_and_b64 s[12:13], s[12:13], s[84:85]
	s_or_b64 s[12:13], vcc, s[12:13]
	v_cndmask_b32_e64 v88, 0, 1, s[12:13]
	v_add3_u32 v86, v86, v87, v88
	ds_bpermute_b32 v87, v48, v85
	ds_bpermute_b32 v88, v47, v85
	v_or_b32_e32 v38, 0x7c, v35
	ds_bpermute_b32 v89, v38, v85
	s_waitcnt lgkmcnt(2)
	v_cmp_eq_f32_e64 s[12:13], v85, v87
	v_cmp_lt_f32_e32 vcc, v85, v87
	s_and_b64 s[12:13], s[12:13], s[86:87]
	s_or_b64 s[12:13], vcc, s[12:13]
	v_cndmask_b32_e64 v87, 0, 1, s[12:13]
	s_waitcnt lgkmcnt(1)
	v_cmp_eq_f32_e64 s[12:13], v85, v88
	v_cmp_lt_f32_e32 vcc, v85, v88
	s_and_b64 s[12:13], s[12:13], s[88:89]
	s_or_b64 s[12:13], vcc, s[12:13]
	v_cndmask_b32_e64 v88, 0, 1, s[12:13]
	v_add3_u32 v86, v86, v87, v88
	ds_bpermute_b32 v87, v46, v85
	ds_bpermute_b32 v88, v45, v85
	s_waitcnt lgkmcnt(1)
	v_cmp_eq_f32_e64 s[12:13], v85, v87
	v_cmp_lt_f32_e32 vcc, v85, v87
	s_and_b64 s[12:13], s[12:13], s[90:91]
	s_or_b64 s[12:13], vcc, s[12:13]
	v_cndmask_b32_e64 v87, 0, 1, s[12:13]
	s_waitcnt lgkmcnt(0)
	v_cmp_eq_f32_e64 s[12:13], v85, v88
	v_cmp_lt_f32_e32 vcc, v85, v88
	s_and_b64 s[12:13], s[12:13], s[94:95]
	s_or_b64 s[12:13], vcc, s[12:13]
	v_cndmask_b32_e64 v88, 0, 1, s[12:13]
	v_add3_u32 v86, v86, v87, v88
	ds_bpermute_b32 v87, v44, v85
	ds_bpermute_b32 v88, v43, v85
	s_waitcnt lgkmcnt(1)
	v_cmp_eq_f32_e64 s[12:13], v85, v87
	v_cmp_lt_f32_e32 vcc, v85, v87
	s_and_b64 s[12:13], s[12:13], s[96:97]
	s_or_b64 s[12:13], vcc, s[12:13]
	v_cndmask_b32_e64 v87, 0, 1, s[12:13]
	s_waitcnt lgkmcnt(0)
	v_cmp_eq_f32_e64 s[12:13], v85, v88
	v_cmp_lt_f32_e32 vcc, v85, v88
	s_and_b64 s[12:13], s[12:13], s[6:7]
	s_or_b64 s[12:13], vcc, s[12:13]
	v_cndmask_b32_e64 v88, 0, 1, s[12:13]
	v_add3_u32 v86, v86, v87, v88
	ds_bpermute_b32 v87, v42, v85
	ds_bpermute_b32 v88, v41, v85
	s_waitcnt lgkmcnt(1)
	v_cmp_eq_f32_e64 s[12:13], v85, v87
	v_cmp_lt_f32_e32 vcc, v85, v87
	s_and_b64 s[12:13], s[12:13], s[4:5]
	s_or_b64 s[12:13], vcc, s[12:13]
	v_cndmask_b32_e64 v87, 0, 1, s[12:13]
	s_waitcnt lgkmcnt(0)
	v_cmp_eq_f32_e64 s[12:13], v85, v88
	v_cmp_lt_f32_e32 vcc, v85, v88
	s_and_b64 s[12:13], s[12:13], s[10:11]
	s_or_b64 s[12:13], vcc, s[12:13]
	v_cndmask_b32_e64 v88, 0, 1, s[12:13]
	v_add3_u32 v86, v86, v87, v88
	ds_bpermute_b32 v87, v40, v85
	ds_bpermute_b32 v88, v39, v85
	s_waitcnt lgkmcnt(1)
	v_cmp_eq_f32_e64 s[12:13], v85, v87
	v_cmp_lt_f32_e32 vcc, v85, v87
	s_and_b64 s[12:13], s[12:13], s[8:9]
	s_or_b64 s[12:13], vcc, s[12:13]
	v_cndmask_b32_e64 v87, 0, 1, s[12:13]
	s_waitcnt lgkmcnt(0)
	v_cmp_eq_f32_e64 s[12:13], v85, v88
	v_cmp_lt_f32_e32 vcc, v85, v88
	s_and_b64 s[12:13], s[66:67], s[12:13]
	s_or_b64 s[12:13], vcc, s[12:13]
	v_cmp_lt_f32_e32 vcc, v85, v89
	v_cndmask_b32_e64 v88, 0, 1, s[12:13]
	s_nop 0
	v_addc_co_u32_e32 v85, vcc, v86, v87, vcc
	v_add_u32_e32 v85, v85, v88
	v_cmp_gt_u32_e32 vcc, 16, v85
	s_and_saveexec_b64 s[12:13], s[44:45]
	v_lshl_add_u32 v84, v84, 2, 0
	v_lshrrev_b64 v[86:87], v34, vcc
	v_add_u32_e32 v84, 0x1d400, v84
	ds_write_b32 v84, v86
	s_or_b64 exec, exec, s[12:13]
	v_add_u32_e32 v84, 32, v37
	v_lshl_or_b32 v85, v84, 5, v73
	v_add_u32_e32 v217, v84, v73
	v_add_u32_e32 v218, -1, v217
	v_and_b32_e32 v217, 31, v217
	v_and_b32_e32 v218, 31, v218
	v_lshl_or_b32 v217, v84, 5, v217
	v_lshl_or_b32 v218, v84, 5, v218
	v_lshl_add_u32 v86, v217, 2, 0
	ds_read_b32 v87, v86 offset:54272
	s_waitcnt lgkmcnt(0)
	v_add_f32_e32 v87, 0, v87
	s_and_saveexec_b64 s[12:13], s[0:1]
	s_cbranch_execz .LBB0_438
	v_lshlrev_b32_e32 v88, 2, v85
	s_add_i32 s14, 0, 0x15400
	v_lshl_add_u32 v88, v218, 2, s14
	ds_read_b32 v88, v88
	s_waitcnt lgkmcnt(0)
	v_add_f32_e32 v87, v87, v88
.LBB0_438:
	s_or_b64 exec, exec, s[12:13]
	ds_read_b32 v88, v86 offset:62464
	s_waitcnt lgkmcnt(0)
	v_add_f32_e32 v87, v87, v88
	s_and_saveexec_b64 s[12:13], s[0:1]
	s_cbranch_execz .LBB0_440
	s_add_i32 s14, 0, 0x15400
	v_lshl_add_u32 v88, v218, 2, s14
	ds_read_b32 v88, v88 offset:8192
	s_waitcnt lgkmcnt(0)
	v_add_f32_e32 v87, v87, v88
.LBB0_440:
	s_or_b64 exec, exec, s[12:13]
	v_add_u32_e32 v86, 0xd400, v86
	ds_read_b32 v88, v86 offset:16384
	s_waitcnt lgkmcnt(0)
	v_add_f32_e32 v87, v87, v88
	s_and_saveexec_b64 s[12:13], s[0:1]
	s_cbranch_execz .LBB0_442
	s_add_i32 s14, 0, 0x15400
	v_lshl_add_u32 v88, v218, 2, s14
	ds_read_b32 v88, v88 offset:16384
	s_waitcnt lgkmcnt(0)
	v_add_f32_e32 v87, v87, v88
; __device__ __forceinline__ void unit(LAS unsigned char* lds, const bf16* Z, const bf16* kct, const bf16* vct, bf16* OAp, int b, int g, int iq, const int tid_in) {
;     ...
;         for (int q = 0; q < 4; ++q) { const int tk = (tid >> 5) + 16 * q;
;             float imp = 0.f;
; #pragma unroll
;             for (int jj = 0; jj < 4; ++jj) { imp += IA[(jj * 64 + tk) * 32 + n]; if (n > 0) imp += IB[(jj * 64 + tk) * 32 + n - 1]; }
;             const bool valid = n <= iq, forced = (n == 0) || (n == iq) || (n == iq - 1);
;             const float sc = forced ? 1e4f : (valid ? imp : -1.0f);
;             int cnt = 0;
; #pragma unroll
;             for (int mm = 0; mm < 32; ++mm) { const float so = __shfl(sc, (lane & 32) + mm); cnt += (so > sc || (so == sc && mm < n)) ? 1 : 0; }
.LBB0_442:
	s_or_b64 exec, exec, s[12:13]
	ds_read_b32 v86, v86 offset:24576
	s_waitcnt lgkmcnt(0)
	v_add_f32_e32 v86, v87, v86
	s_and_saveexec_b64 s[12:13], s[0:1]
	s_cbranch_execz .LBB0_444
	s_add_i32 s14, 0, 0x15400
	v_lshl_add_u32 v85, v218, 2, s14
	ds_read_b32 v85, v85 offset:24576
	s_waitcnt lgkmcnt(0)
	v_add_f32_e32 v86, v86, v85
.LBB0_444:
	s_or_b64 exec, exec, s[12:13]
	v_cndmask_b32_e64 v85, v86, -1.0, s[38:39]
	v_cndmask_b32_e64 v85, v85, v230, s[40:41]
	ds_bpermute_b32 v86, v35, v85
	ds_bpermute_b32 v87, v83, v85
	ds_bpermute_b32 v88, v82, v85
	ds_bpermute_b32 v89, v38, v85
	s_waitcnt lgkmcnt(3)
	v_cmp_eq_f32_e64 s[12:13], v85, v86
	v_cmp_lt_f32_e32 vcc, v85, v86
	s_and_b64 s[12:13], s[56:57], s[12:13]
	s_or_b64 s[12:13], vcc, s[12:13]
	v_cndmask_b32_e64 v86, 0, 1, s[12:13]
	s_waitcnt lgkmcnt(2)
	v_cmp_eq_f32_e64 s[12:13], v85, v87
	v_cmp_lt_f32_e32 vcc, v85, v87
	s_and_b64 s[12:13], s[12:13], s[92:93]
	s_or_b64 s[12:13], vcc, s[12:13]
	v_cndmask_b32_e64 v87, 0, 1, s[12:13]
	s_waitcnt lgkmcnt(1)
	v_cmp_eq_f32_e64 s[12:13], v85, v88
	v_cmp_lt_f32_e32 vcc, v85, v88
	s_and_b64 s[12:13], s[12:13], s[50:51]
	s_or_b64 s[12:13], vcc, s[12:13]
	v_cndmask_b32_e64 v88, 0, 1, s[12:13]
	v_add3_u32 v86, v86, v87, v88
	ds_bpermute_b32 v87, v81, v85
	ds_bpermute_b32 v88, v67, v85
	s_waitcnt lgkmcnt(1)
	v_cmp_eq_f32_e64 s[12:13], v85, v87
	v_cmp_lt_f32_e32 vcc, v85, v87
	s_and_b64 s[12:13], s[12:13], s[42:43]
	s_or_b64 s[12:13], vcc, s[12:13]
	v_cndmask_b32_e64 v87, 0, 1, s[12:13]
	s_waitcnt lgkmcnt(0)
	v_cmp_eq_f32_e64 s[12:13], v85, v88
	v_cmp_lt_f32_e32 vcc, v85, v88
	s_and_b64 s[12:13], s[12:13], s[46:47]
	s_or_b64 s[12:13], vcc, s[12:13]
	v_cndmask_b32_e64 v88, 0, 1, s[12:13]
	v_add3_u32 v86, v86, v87, v88
	ds_bpermute_b32 v87, v66, v85
	ds_bpermute_b32 v88, v65, v85
	s_waitcnt lgkmcnt(1)
	v_cmp_eq_f32_e64 s[12:13], v85, v87
	v_cmp_lt_f32_e32 vcc, v85, v87
	s_and_b64 s[12:13], s[12:13], s[48:49]
	s_or_b64 s[12:13], vcc, s[12:13]
	v_cndmask_b32_e64 v87, 0, 1, s[12:13]
	s_waitcnt lgkmcnt(0)
	v_cmp_eq_f32_e64 s[12:13], v85, v88
	v_cmp_lt_f32_e32 vcc, v85, v88
	s_and_b64 s[12:13], s[12:13], s[52:53]
	s_or_b64 s[12:13], vcc, s[12:13]
	v_cndmask_b32_e64 v88, 0, 1, s[12:13]
	v_add3_u32 v86, v86, v87, v88
	ds_bpermute_b32 v87, v64, v85
	ds_bpermute_b32 v88, v63, v85
	s_waitcnt lgkmcnt(1)
	v_cmp_eq_f32_e64 s[12:13], v85, v87
	v_cmp_lt_f32_e32 vcc, v85, v87
	s_and_b64 s[12:13], s[12:13], s[54:55]
	s_or_b64 s[12:13], vcc, s[12:13]
	v_cndmask_b32_e64 v87, 0, 1, s[12:13]
	s_waitcnt lgkmcnt(0)
	v_cmp_eq_f32_e64 s[12:13], v85, v88
	v_cmp_lt_f32_e32 vcc, v85, v88
	s_and_b64 s[12:13], s[12:13], s[58:59]
	s_or_b64 s[12:13], vcc, s[12:13]
	v_cndmask_b32_e64 v88, 0, 1, s[12:13]
	v_add3_u32 v86, v86, v87, v88
	ds_bpermute_b32 v87, v62, v85
	ds_bpermute_b32 v88, v61, v85
	s_waitcnt lgkmcnt(1)
	v_cmp_eq_f32_e64 s[12:13], v85, v87
	v_cmp_lt_f32_e32 vcc, v85, v87
	s_and_b64 s[12:13], s[12:13], s[60:61]
	s_or_b64 s[12:13], vcc, s[12:13]
	v_cndmask_b32_e64 v87, 0, 1, s[12:13]
	s_waitcnt lgkmcnt(0)
	v_cmp_eq_f32_e64 s[12:13], v85, v88
	v_cmp_lt_f32_e32 vcc, v85, v88
	s_and_b64 s[12:13], s[12:13], s[62:63]
	s_or_b64 s[12:13], vcc, s[12:13]
	v_cndmask_b32_e64 v88, 0, 1, s[12:13]
	v_add3_u32 v86, v86, v87, v88
	ds_bpermute_b32 v87, v60, v85
	ds_bpermute_b32 v88, v59, v85
	s_waitcnt lgkmcnt(1)
	v_cmp_eq_f32_e64 s[12:13], v85, v87
	v_cmp_lt_f32_e32 vcc, v85, v87
	s_and_b64 s[12:13], s[12:13], s[64:65]
	s_or_b64 s[12:13], vcc, s[12:13]
	v_cndmask_b32_e64 v87, 0, 1, s[12:13]
	s_waitcnt lgkmcnt(0)
	v_cmp_eq_f32_e64 s[12:13], v85, v88
	v_cmp_lt_f32_e32 vcc, v85, v88
	s_and_b64 s[12:13], s[12:13], s[68:69]
	s_or_b64 s[12:13], vcc, s[12:13]
	v_cndmask_b32_e64 v88, 0, 1, s[12:13]
	v_add3_u32 v86, v86, v87, v88
	ds_bpermute_b32 v87, v58, v85
	ds_bpermute_b32 v88, v57, v85
	s_waitcnt lgkmcnt(1)
	v_cmp_eq_f32_e64 s[12:13], v85, v87
	v_cmp_lt_f32_e32 vcc, v85, v87
	s_and_b64 s[12:13], s[12:13], s[70:71]
	s_or_b64 s[12:13], vcc, s[12:13]
	v_cndmask_b32_e64 v87, 0, 1, s[12:13]
	s_waitcnt lgkmcnt(0)
	v_cmp_eq_f32_e64 s[12:13], v85, v88
	v_cmp_lt_f32_e32 vcc, v85, v88
	s_and_b64 s[12:13], s[12:13], s[72:73]
	s_or_b64 s[12:13], vcc, s[12:13]
	v_cndmask_b32_e64 v88, 0, 1, s[12:13]
	v_add3_u32 v86, v86, v87, v88
	ds_bpermute_b32 v87, v56, v85
	ds_bpermute_b32 v88, v55, v85
	s_waitcnt lgkmcnt(1)
	v_cmp_eq_f32_e64 s[12:13], v85, v87
	v_cmp_lt_f32_e32 vcc, v85, v87
	s_and_b64 s[12:13], s[12:13], s[74:75]
	s_or_b64 s[12:13], vcc, s[12:13]
	v_cndmask_b32_e64 v87, 0, 1, s[12:13]
	s_waitcnt lgkmcnt(0)
	v_cmp_eq_f32_e64 s[12:13], v85, v88
	v_cmp_lt_f32_e32 vcc, v85, v88
	s_and_b64 s[12:13], s[12:13], s[76:77]
	s_or_b64 s[12:13], vcc, s[12:13]
	v_cndmask_b32_e64 v88, 0, 1, s[12:13]
	v_add3_u32 v86, v86, v87, v88
	ds_bpermute_b32 v87, v54, v85
	ds_bpermute_b32 v88, v53, v85
	s_waitcnt lgkmcnt(1)
	v_cmp_eq_f32_e64 s[12:13], v85, v87
	v_cmp_lt_f32_e32 vcc, v85, v87
	s_and_b64 s[12:13], s[12:13], s[78:79]
	s_or_b64 s[12:13], vcc, s[12:13]
	v_cndmask_b32_e64 v87, 0, 1, s[12:13]
	s_waitcnt lgkmcnt(0)
; __device__ __forceinline__ void unit(LAS unsigned char* lds, const bf16* Z, const bf16* kct, const bf16* vct, bf16* OAp, int b, int g, int iq, const int tid_in) {
;     ...
;         for (int q = 0; q < 4; ++q) { const int tk = (tid >> 5) + 16 * q;
;             float imp = 0.f;
; #pragma unroll
;             for (int jj = 0; jj < 4; ++jj) { imp += IA[(jj * 64 + tk) * 32 + n]; if (n > 0) imp += IB[(jj * 64 + tk) * 32 + n - 1]; }
;             const bool valid = n <= iq, forced = (n == 0) || (n == iq) || (n == iq - 1);
;             const float sc = forced ? 1e4f : (valid ? imp : -1.0f);
;             int cnt = 0;
; #pragma unroll
;             for (int mm = 0; mm < 32; ++mm) { const float so = __shfl(sc, (lane & 32) + mm); cnt += (so > sc || (so == sc && mm < n)) ? 1 : 0; }
;             const unsigned long long bal = __ballot(cnt < 16);
;             if (n == 0) MSK[tk] = (unsigned)((lane & 32) ? (bal >> 32) : bal); }
	v_cmp_eq_f32_e64 s[12:13], v85, v88
	v_cmp_lt_f32_e32 vcc, v85, v88
	s_and_b64 s[12:13], s[12:13], s[80:81]
	s_or_b64 s[12:13], vcc, s[12:13]
	v_cndmask_b32_e64 v88, 0, 1, s[12:13]
	v_add3_u32 v86, v86, v87, v88
	ds_bpermute_b32 v87, v52, v85
	ds_bpermute_b32 v88, v49, v85
	s_waitcnt lgkmcnt(1)
	v_cmp_eq_f32_e64 s[12:13], v85, v87
	v_cmp_lt_f32_e32 vcc, v85, v87
	s_and_b64 s[12:13], s[12:13], s[82:83]
	s_or_b64 s[12:13], vcc, s[12:13]
	v_cndmask_b32_e64 v87, 0, 1, s[12:13]
	s_waitcnt lgkmcnt(0)
	v_cmp_eq_f32_e64 s[12:13], v85, v88
	v_cmp_lt_f32_e32 vcc, v85, v88
	s_and_b64 s[12:13], s[12:13], s[84:85]
	s_or_b64 s[12:13], vcc, s[12:13]
	v_cndmask_b32_e64 v88, 0, 1, s[12:13]
	v_add3_u32 v86, v86, v87, v88
	ds_bpermute_b32 v87, v48, v85
	ds_bpermute_b32 v88, v47, v85
	s_waitcnt lgkmcnt(1)
	v_cmp_eq_f32_e64 s[12:13], v85, v87
	v_cmp_lt_f32_e32 vcc, v85, v87
	s_and_b64 s[12:13], s[12:13], s[86:87]
	s_or_b64 s[12:13], vcc, s[12:13]
	v_cndmask_b32_e64 v87, 0, 1, s[12:13]
	s_waitcnt lgkmcnt(0)
	v_cmp_eq_f32_e64 s[12:13], v85, v88
	v_cmp_lt_f32_e32 vcc, v85, v88
	s_and_b64 s[12:13], s[12:13], s[88:89]
	s_or_b64 s[12:13], vcc, s[12:13]
	v_cndmask_b32_e64 v88, 0, 1, s[12:13]
	v_add3_u32 v86, v86, v87, v88
	ds_bpermute_b32 v87, v46, v85
	ds_bpermute_b32 v88, v45, v85
	s_waitcnt lgkmcnt(1)
	v_cmp_eq_f32_e64 s[12:13], v85, v87
	v_cmp_lt_f32_e32 vcc, v85, v87
	s_and_b64 s[12:13], s[12:13], s[90:91]
	s_or_b64 s[12:13], vcc, s[12:13]
	v_cndmask_b32_e64 v87, 0, 1, s[12:13]
	s_waitcnt lgkmcnt(0)
	v_cmp_eq_f32_e64 s[12:13], v85, v88
	v_cmp_lt_f32_e32 vcc, v85, v88
	s_and_b64 s[12:13], s[12:13], s[94:95]
	s_or_b64 s[12:13], vcc, s[12:13]
	v_cndmask_b32_e64 v88, 0, 1, s[12:13]
	v_add3_u32 v86, v86, v87, v88
	ds_bpermute_b32 v87, v44, v85
	ds_bpermute_b32 v88, v43, v85
	s_waitcnt lgkmcnt(1)
	v_cmp_eq_f32_e64 s[12:13], v85, v87
	v_cmp_lt_f32_e32 vcc, v85, v87
	s_and_b64 s[12:13], s[12:13], s[96:97]
	s_or_b64 s[12:13], vcc, s[12:13]
	v_cndmask_b32_e64 v87, 0, 1, s[12:13]
	s_waitcnt lgkmcnt(0)
	v_cmp_eq_f32_e64 s[12:13], v85, v88
	v_cmp_lt_f32_e32 vcc, v85, v88
	s_and_b64 s[12:13], s[12:13], s[6:7]
	s_or_b64 s[12:13], vcc, s[12:13]
	v_cndmask_b32_e64 v88, 0, 1, s[12:13]
	v_add3_u32 v86, v86, v87, v88
	ds_bpermute_b32 v87, v42, v85
	ds_bpermute_b32 v88, v41, v85
	s_waitcnt lgkmcnt(1)
	v_cmp_eq_f32_e64 s[12:13], v85, v87
	v_cmp_lt_f32_e32 vcc, v85, v87
	s_and_b64 s[12:13], s[12:13], s[4:5]
	s_or_b64 s[12:13], vcc, s[12:13]
	v_cndmask_b32_e64 v87, 0, 1, s[12:13]
	s_waitcnt lgkmcnt(0)
	v_cmp_eq_f32_e64 s[12:13], v85, v88
	v_cmp_lt_f32_e32 vcc, v85, v88
	s_and_b64 s[12:13], s[12:13], s[10:11]
	s_or_b64 s[12:13], vcc, s[12:13]
	v_cndmask_b32_e64 v88, 0, 1, s[12:13]
	v_add3_u32 v86, v86, v87, v88
	ds_bpermute_b32 v87, v40, v85
	ds_bpermute_b32 v88, v39, v85
	s_waitcnt lgkmcnt(1)
	v_cmp_eq_f32_e64 s[12:13], v85, v87
	v_cmp_lt_f32_e32 vcc, v85, v87
	s_and_b64 s[12:13], s[12:13], s[8:9]
	s_or_b64 s[12:13], vcc, s[12:13]
	v_cndmask_b32_e64 v87, 0, 1, s[12:13]
	s_waitcnt lgkmcnt(0)
	v_cmp_eq_f32_e64 s[12:13], v85, v88
	v_cmp_lt_f32_e32 vcc, v85, v88
	s_and_b64 s[12:13], s[66:67], s[12:13]
	s_or_b64 s[12:13], vcc, s[12:13]
	v_cmp_lt_f32_e32 vcc, v85, v89
	v_cndmask_b32_e64 v88, 0, 1, s[12:13]
	s_nop 0
	v_addc_co_u32_e32 v85, vcc, v86, v87, vcc
	v_add_u32_e32 v85, v85, v88
	v_cmp_gt_u32_e32 vcc, 16, v85
	s_and_saveexec_b64 s[12:13], s[44:45]
	v_lshl_add_u32 v84, v84, 2, 0
	v_lshrrev_b64 v[86:87], v34, vcc
	v_add_u32_e32 v84, 0x1d400, v84
	ds_write_b32 v84, v86
	s_or_b64 exec, exec, s[12:13]
	v_add_u32_e32 v37, 48, v37
	v_lshl_or_b32 v84, v37, 5, v73
	v_add_u32_e32 v217, v37, v73
	v_add_u32_e32 v218, -1, v217
	v_and_b32_e32 v217, 31, v217
	v_and_b32_e32 v218, 31, v218
	v_lshl_or_b32 v217, v37, 5, v217
	v_lshl_or_b32 v218, v37, 5, v218
	v_lshl_add_u32 v85, v217, 2, 0
	ds_read_b32 v86, v85 offset:54272
	s_waitcnt lgkmcnt(0)
	v_add_f32_e32 v86, 0, v86
	s_and_saveexec_b64 s[12:13], s[0:1]
	s_cbranch_execz .LBB0_448
	v_lshlrev_b32_e32 v87, 2, v84
	s_add_i32 s14, 0, 0x15400
	v_lshl_add_u32 v87, v218, 2, s14
	ds_read_b32 v87, v87
	s_waitcnt lgkmcnt(0)
	v_add_f32_e32 v86, v86, v87
.LBB0_448:
	s_or_b64 exec, exec, s[12:13]
	ds_read_b32 v87, v85 offset:62464
	s_waitcnt lgkmcnt(0)
	v_add_f32_e32 v86, v86, v87
	s_and_saveexec_b64 s[12:13], s[0:1]
	s_cbranch_execz .LBB0_450
	s_add_i32 s14, 0, 0x15400
	v_lshl_add_u32 v87, v218, 2, s14
	ds_read_b32 v87, v87 offset:8192
	s_waitcnt lgkmcnt(0)
	v_add_f32_e32 v86, v86, v87
.LBB0_450:
	s_or_b64 exec, exec, s[12:13]
	v_add_u32_e32 v85, 0xd400, v85
	ds_read_b32 v87, v85 offset:16384
	s_waitcnt lgkmcnt(0)
	v_add_f32_e32 v86, v86, v87
	s_and_saveexec_b64 s[12:13], s[0:1]
	s_cbranch_execz .LBB0_452
	s_add_i32 s14, 0, 0x15400
	v_lshl_add_u32 v87, v218, 2, s14
	ds_read_b32 v87, v87 offset:16384
	s_waitcnt lgkmcnt(0)
	v_add_f32_e32 v86, v86, v87
.LBB0_452:
	s_or_b64 exec, exec, s[12:13]
	ds_read_b32 v85, v85 offset:24576
	s_waitcnt lgkmcnt(0)
	v_add_f32_e32 v85, v86, v85
	s_and_saveexec_b64 s[12:13], s[0:1]
	s_cbranch_execz .LBB0_454
	s_add_i32 s0, 0, 0x15400
	v_lshl_add_u32 v84, v218, 2, s0
	ds_read_b32 v84, v84 offset:24576
	s_waitcnt lgkmcnt(0)
	v_add_f32_e32 v85, v85, v84
